# c7 + post-loop MFMA wait-state pad s_nop 15x2 -> s_nop 7 (fp8 GEMM phases)
# speedup vs baseline: 1.0116x; 1.0053x over previous
; __device__ __forceinline__ unsigned cvt_pk_bf16(float lo, float hi) { const f32x2 v = {lo, hi}; const bf16x2_t b = __builtin_convertvector(v, bf16x2_t); return __builtin_bit_cast(unsigned, b); }
; #define PG8_SCHED __builtin_amdgcn_sched_barrier(0)
; __device__ __forceinline__ unsigned long long rt() { return __builtin_amdgcn_s_memrealtime(); }
;     __device__ __forceinline__ void operator()(const f32x4 (&acc)[2][2][4][2], const Unit& u, int wr, int wc, int fr, int fq) const {
;         const int row0 = u.pm * BM + wr * 64 + fr, col0 = u.pn * BM + wc * 32 + 8 * fq;
;         const float sc0 = ((smask >> (2 * u.pn)) & 1u) ? sval : 1.0f, sc1 = ((smask >> (2 * u.pn + 1)) & 1u) ? sval : 1.0f;
; #pragma unroll
;         for (int ai = 0; ai < 2; ++ai)
; #pragma unroll
;             for (int m = 0; m < 4; ++m) { bf16_t* rowp = O + (size_t)(row0 + ai * HALF + m * 16) * ldc + col0;
;                 const float rs = rt ? rt[ai * HALF + wr * 64 + m * 16 + fr] : 1.0f;
; #pragma unroll
;                 for (int bj = 0; bj < 2; ++bj) { const float sc = (bj ? sc1 : sc0) * rs; const f32x4 v0 = acc[ai][bj][m][0] * sc, v1 = acc[ai][bj][m][1] * sc;
;                     u32x4 w; w.x = cvt_pk_bf16(v0[0], v0[1]); w.y = cvt_pk_bf16(v0[2], v0[3]); w.z = cvt_pk_bf16(v1[0], v1[1]); w.w = cvt_pk_bf16(v1[2], v1[3]);
;                     *(u32x4*)(rowp + bj * HALF) = w; } }
; template <class Epi, class Sched, bool ALIGN_EPI = false, bool SP2 = false, bool F8 = false>
; __device__ __forceinline__ void gemm_phase(PG8_LAS unsigned char* lds, const Gemm g, const Sched& S, const Epi& E) {
;     ...
;         if constexpr (F8) { asm volatile("s_nop 15\n\ts_nop 15" ::: "memory"); PG8_SCHED; }
.LBB0_154:
	s_nop 7
	s_lshl_b32 s0, s90, 1
	s_lshl_b32 s1, 1, s0
	s_and_b32 s1, s1, 0x415
	s_cmp_eq_u32 s1, 0
	s_cselect_b64 s[4:5], -1, 0
	s_lshl_b32 s0, 2, s0
	ds_read2_b32 v[10:11], v191 offset1:16
	s_and_b32 s0, s0, 0x22a
	v_lshl_or_b32 v4, s90, 8, v193
	s_cmp_eq_u32 s0, 0
	v_lshl_add_u32 v20, s44, 8, v165
	v_cndmask_b32_e64 v21, v198, 1.0, s[4:5]
	s_cselect_b64 s[4:5], -1, 0
	v_ashrrev_i32_e32 v5, 31, v4
	v_mov_b64_e32 v[2:3], s[16:17]
	v_cndmask_b32_e64 v22, v198, 1.0, s[4:5]
	v_mad_i64_i32 v[6:7], s[4:5], v20, s89, v[2:3]
	v_lshlrev_b64 v[4:5], 1, v[4:5]
	v_lshl_add_u64 v[12:13], v[6:7], 0, v[4:5]
	s_waitcnt lgkmcnt(0)
	v_mul_f32_e32 v6, v21, v10
	v_pk_mul_f32 v[8:9], v[160:161], v[6:7] op_sel_hi:[1,0]
	v_pk_mul_f32 v[14:15], v[158:159], v[6:7] op_sel_hi:[1,0]
	v_pk_mul_f32 v[16:17], v[156:157], v[6:7] op_sel_hi:[1,0]
	v_pk_mul_f32 v[18:19], v[154:155], v[6:7] op_sel_hi:[1,0]
	v_cvt_pk_bf16_f32 v6, v14, v15
	v_cvt_pk_bf16_f32 v7, v8, v9
	v_cvt_pk_bf16_f32 v8, v18, v19
	v_cvt_pk_bf16_f32 v9, v16, v17
	global_store_dwordx4 v[12:13], v[6:9], off
	s_andn2_b64 vcc, exec, s[8:9]
	s_mov_b64 s[8:9], -1
	v_mul_f32_e32 v6, v22, v10
	v_pk_mul_f32 v[8:9], v[148:149], v[6:7] op_sel_hi:[1,0]
	v_pk_mul_f32 v[14:15], v[146:147], v[6:7] op_sel_hi:[1,0]
	v_pk_mul_f32 v[16:17], v[140:141], v[6:7] op_sel_hi:[1,0]
	v_pk_mul_f32 v[18:19], v[138:139], v[6:7] op_sel_hi:[1,0]
	v_cvt_pk_bf16_f32 v6, v14, v15
	v_cvt_pk_bf16_f32 v7, v8, v9
	v_cvt_pk_bf16_f32 v8, v18, v19
	v_cvt_pk_bf16_f32 v9, v16, v17
	global_store_dwordx4 v[12:13], v[6:9], off offset:256
	ds_read_b32 v23, v191 offset:704
	s_nop 0
	v_or_b32_e32 v6, 16, v20
	v_mad_i64_i32 v[6:7], s[4:5], v6, s89, v[2:3]
	v_lshl_add_u64 v[12:13], v[6:7], 0, v[4:5]
	v_mul_f32_e32 v6, v21, v11
	v_pk_mul_f32 v[8:9], v[152:153], v[6:7] op_sel_hi:[1,0]
	v_pk_mul_f32 v[14:15], v[150:151], v[6:7] op_sel_hi:[1,0]
	v_pk_mul_f32 v[16:17], v[144:145], v[6:7] op_sel_hi:[1,0]
	v_pk_mul_f32 v[18:19], v[142:143], v[6:7] op_sel_hi:[1,0]
	v_cvt_pk_bf16_f32 v6, v14, v15
	v_cvt_pk_bf16_f32 v7, v8, v9
	v_cvt_pk_bf16_f32 v8, v18, v19
	v_cvt_pk_bf16_f32 v9, v16, v17
	global_store_dwordx4 v[12:13], v[6:9], off
	s_nop 1
	v_mul_f32_e32 v6, v22, v11
	v_pk_mul_f32 v[10:11], v[134:135], v[6:7] op_sel_hi:[1,0]
	v_pk_mul_f32 v[8:9], v[136:137], v[6:7] op_sel_hi:[1,0]
	v_pk_mul_f32 v[14:15], v[128:129], v[6:7] op_sel_hi:[1,0]
	v_pk_mul_f32 v[16:17], v[126:127], v[6:7] op_sel_hi:[1,0]
	v_cvt_pk_bf16_f32 v6, v10, v11
	ds_read2_b32 v[10:11], v191 offset0:32 offset1:48
	v_cvt_pk_bf16_f32 v7, v8, v9
	v_cvt_pk_bf16_f32 v8, v16, v17
	v_cvt_pk_bf16_f32 v9, v14, v15
	global_store_dwordx4 v[12:13], v[6:9], off offset:256
	s_nop 1
	v_or_b32_e32 v6, 32, v20
	v_mad_i64_i32 v[6:7], s[4:5], v6, s89, v[2:3]
	v_lshl_add_u64 v[12:13], v[6:7], 0, v[4:5]
	s_waitcnt lgkmcnt(0)
	v_mul_f32_e32 v6, v21, v10
	v_pk_mul_f32 v[8:9], v[132:133], v[6:7] op_sel_hi:[1,0]
	v_pk_mul_f32 v[14:15], v[130:131], v[6:7] op_sel_hi:[1,0]
	v_pk_mul_f32 v[16:17], v[124:125], v[6:7] op_sel_hi:[1,0]
	v_pk_mul_f32 v[18:19], v[122:123], v[6:7] op_sel_hi:[1,0]
	v_cvt_pk_bf16_f32 v6, v14, v15
	v_cvt_pk_bf16_f32 v7, v8, v9
	v_cvt_pk_bf16_f32 v8, v18, v19
	v_cvt_pk_bf16_f32 v9, v16, v17
	global_store_dwordx4 v[12:13], v[6:9], off
	s_nop 1
	v_mul_f32_e32 v6, v22, v10
	v_pk_mul_f32 v[8:9], v[116:117], v[6:7] op_sel_hi:[1,0]
	v_pk_mul_f32 v[14:15], v[114:115], v[6:7] op_sel_hi:[1,0]
	v_pk_mul_f32 v[16:17], v[108:109], v[6:7] op_sel_hi:[1,0]
	v_pk_mul_f32 v[18:19], v[106:107], v[6:7] op_sel_hi:[1,0]
	v_cvt_pk_bf16_f32 v6, v14, v15
	v_cvt_pk_bf16_f32 v7, v8, v9
	v_cvt_pk_bf16_f32 v8, v18, v19
	v_cvt_pk_bf16_f32 v9, v16, v17
	global_store_dwordx4 v[12:13], v[6:9], off offset:256
	s_nop 1
	v_or_b32_e32 v6, 48, v20
	v_mad_i64_i32 v[6:7], s[4:5], v6, s89, v[2:3]
	v_lshl_add_u64 v[12:13], v[6:7], 0, v[4:5]
	v_mul_f32_e32 v6, v21, v11
	v_pk_mul_f32 v[8:9], v[120:121], v[6:7] op_sel_hi:[1,0]
	v_pk_mul_f32 v[14:15], v[118:119], v[6:7] op_sel_hi:[1,0]
	v_pk_mul_f32 v[16:17], v[112:113], v[6:7] op_sel_hi:[1,0]
	v_pk_mul_f32 v[18:19], v[110:111], v[6:7] op_sel_hi:[1,0]
	v_cvt_pk_bf16_f32 v6, v14, v15
	v_cvt_pk_bf16_f32 v7, v8, v9
	v_cvt_pk_bf16_f32 v8, v18, v19
	v_cvt_pk_bf16_f32 v9, v16, v17
	global_store_dwordx4 v[12:13], v[6:9], off
	ds_read_b32 v18, v192
	s_nop 0
	v_mul_f32_e32 v6, v22, v11
	v_pk_mul_f32 v[8:9], v[104:105], v[6:7] op_sel_hi:[1,0]
	v_pk_mul_f32 v[10:11], v[102:103], v[6:7] op_sel_hi:[1,0]
	v_pk_mul_f32 v[14:15], v[100:101], v[6:7] op_sel_hi:[1,0]
	v_pk_mul_f32 v[16:17], v[98:99], v[6:7] op_sel_hi:[1,0]
	v_cvt_pk_bf16_f32 v6, v10, v11
	v_cvt_pk_bf16_f32 v7, v8, v9
	v_cvt_pk_bf16_f32 v8, v16, v17
	v_cvt_pk_bf16_f32 v9, v14, v15
	global_store_dwordx4 v[12:13], v[6:9], off offset:256
	s_nop 1
	v_add_u32_e32 v6, 0x80, v20
	v_mad_i64_i32 v[6:7], s[4:5], v6, s89, v[2:3]
	v_lshl_add_u64 v[10:11], v[6:7], 0, v[4:5]
	s_waitcnt lgkmcnt(0)
; __device__ __forceinline__ unsigned cvt_pk_bf16(float lo, float hi) { const f32x2 v = {lo, hi}; const bf16x2_t b = __builtin_convertvector(v, bf16x2_t); return __builtin_bit_cast(unsigned, b); }
; __device__ __forceinline__ unsigned long long rt() { return __builtin_amdgcn_s_memrealtime(); }
;     __device__ __forceinline__ void operator()(const f32x4 (&acc)[2][2][4][2], const Unit& u, int wr, int wc, int fr, int fq) const {
;     ...
;             for (int m = 0; m < 4; ++m) { bf16_t* rowp = O + (size_t)(row0 + ai * HALF + m * 16) * ldc + col0;
;                 const float rs = rt ? rt[ai * HALF + wr * 64 + m * 16 + fr] : 1.0f;
; #pragma unroll
;                 for (int bj = 0; bj < 2; ++bj) { const float sc = (bj ? sc1 : sc0) * rs; const f32x4 v0 = acc[ai][bj][m][0] * sc, v1 = acc[ai][bj][m][1] * sc;
;                     u32x4 w; w.x = cvt_pk_bf16(v0[0], v0[1]); w.y = cvt_pk_bf16(v0[2], v0[3]); w.z = cvt_pk_bf16(v1[0], v1[1]); w.w = cvt_pk_bf16(v1[2], v1[3]);
;                     *(u32x4*)(rowp + bj * HALF) = w; } }
	v_mul_f32_e32 v6, v21, v18
	v_pk_mul_f32 v[8:9], v[96:97], v[6:7] op_sel_hi:[1,0]
	v_pk_mul_f32 v[12:13], v[94:95], v[6:7] op_sel_hi:[1,0]
	v_pk_mul_f32 v[14:15], v[92:93], v[6:7] op_sel_hi:[1,0]
	v_pk_mul_f32 v[16:17], v[90:91], v[6:7] op_sel_hi:[1,0]
	v_cvt_pk_bf16_f32 v6, v12, v13
	v_cvt_pk_bf16_f32 v7, v8, v9
	v_cvt_pk_bf16_f32 v8, v16, v17
	v_cvt_pk_bf16_f32 v9, v14, v15
	global_store_dwordx4 v[10:11], v[6:9], off
	s_nop 1
	v_mul_f32_e32 v6, v22, v18
	v_pk_mul_f32 v[8:9], v[80:81], v[6:7] op_sel_hi:[1,0]
	v_pk_mul_f32 v[12:13], v[78:79], v[6:7] op_sel_hi:[1,0]
	v_pk_mul_f32 v[14:15], v[76:77], v[6:7] op_sel_hi:[1,0]
	v_pk_mul_f32 v[16:17], v[74:75], v[6:7] op_sel_hi:[1,0]
	v_cvt_pk_bf16_f32 v6, v12, v13
	v_cvt_pk_bf16_f32 v7, v8, v9
	v_cvt_pk_bf16_f32 v8, v16, v17
	v_cvt_pk_bf16_f32 v9, v14, v15
	global_store_dwordx4 v[10:11], v[6:9], off offset:256
	ds_read2_b32 v[10:11], v191 offset0:144 offset1:160
	s_nop 0
	v_add_u32_e32 v6, 0x90, v20
	v_mad_i64_i32 v[6:7], s[4:5], v6, s89, v[2:3]
	v_lshl_add_u64 v[12:13], v[6:7], 0, v[4:5]
	s_waitcnt lgkmcnt(0)
	v_mul_f32_e32 v6, v21, v10
	v_pk_mul_f32 v[8:9], v[88:89], v[6:7] op_sel_hi:[1,0]
	v_pk_mul_f32 v[14:15], v[86:87], v[6:7] op_sel_hi:[1,0]
	v_pk_mul_f32 v[16:17], v[84:85], v[6:7] op_sel_hi:[1,0]
	v_pk_mul_f32 v[18:19], v[82:83], v[6:7] op_sel_hi:[1,0]
	v_cvt_pk_bf16_f32 v6, v14, v15
	v_cvt_pk_bf16_f32 v7, v8, v9
	v_cvt_pk_bf16_f32 v8, v18, v19
	v_cvt_pk_bf16_f32 v9, v16, v17
	global_store_dwordx4 v[12:13], v[6:9], off
	s_nop 1
	v_mul_f32_e32 v6, v22, v10
	v_pk_mul_f32 v[8:9], v[64:65], v[6:7] op_sel_hi:[1,0]
	v_pk_mul_f32 v[14:15], v[62:63], v[6:7] op_sel_hi:[1,0]
	v_pk_mul_f32 v[16:17], v[60:61], v[6:7] op_sel_hi:[1,0]
	v_pk_mul_f32 v[18:19], v[58:59], v[6:7] op_sel_hi:[1,0]
	v_cvt_pk_bf16_f32 v6, v14, v15
	v_cvt_pk_bf16_f32 v7, v8, v9
	v_cvt_pk_bf16_f32 v8, v18, v19
	v_cvt_pk_bf16_f32 v9, v16, v17
	global_store_dwordx4 v[12:13], v[6:9], off offset:256
	s_nop 1
	v_add_u32_e32 v6, 0xa0, v20
	v_mad_i64_i32 v[6:7], s[4:5], v6, s89, v[2:3]
	v_lshl_add_u64 v[12:13], v[6:7], 0, v[4:5]
	v_mul_f32_e32 v6, v21, v11
	v_pk_mul_f32 v[8:9], v[72:73], v[6:7] op_sel_hi:[1,0]
	v_pk_mul_f32 v[14:15], v[70:71], v[6:7] op_sel_hi:[1,0]
	v_pk_mul_f32 v[16:17], v[68:69], v[6:7] op_sel_hi:[1,0]
	v_pk_mul_f32 v[18:19], v[66:67], v[6:7] op_sel_hi:[1,0]
	v_cvt_pk_bf16_f32 v6, v14, v15
	v_cvt_pk_bf16_f32 v7, v8, v9
	v_cvt_pk_bf16_f32 v8, v18, v19
	v_cvt_pk_bf16_f32 v9, v16, v17
	global_store_dwordx4 v[12:13], v[6:9], off
	s_nop 1
	v_mul_f32_e32 v6, v22, v11
	v_pk_mul_f32 v[8:9], v[48:49], v[6:7] op_sel_hi:[1,0]
	v_pk_mul_f32 v[10:11], v[46:47], v[6:7] op_sel_hi:[1,0]
	v_pk_mul_f32 v[14:15], v[44:45], v[6:7] op_sel_hi:[1,0]
	v_pk_mul_f32 v[16:17], v[42:43], v[6:7] op_sel_hi:[1,0]
	v_cvt_pk_bf16_f32 v6, v10, v11
	v_cvt_pk_bf16_f32 v7, v8, v9
	v_cvt_pk_bf16_f32 v8, v16, v17
	v_cvt_pk_bf16_f32 v9, v14, v15
	global_store_dwordx4 v[12:13], v[6:9], off offset:256
	s_nop 1
	v_add_u32_e32 v6, 0xb0, v20
	v_mad_i64_i32 v[2:3], s[4:5], v6, s89, v[2:3]
	v_lshl_add_u64 v[6:7], v[2:3], 0, v[4:5]
	v_mul_f32_e32 v2, v21, v23
	v_pk_mul_f32 v[4:5], v[56:57], v[2:3] op_sel_hi:[1,0]
	v_pk_mul_f32 v[8:9], v[54:55], v[2:3] op_sel_hi:[1,0]
	v_pk_mul_f32 v[10:11], v[52:53], v[2:3] op_sel_hi:[1,0]
	v_pk_mul_f32 v[12:13], v[50:51], v[2:3] op_sel_hi:[1,0]
	v_cvt_pk_bf16_f32 v2, v8, v9
	v_cvt_pk_bf16_f32 v3, v4, v5
	v_cvt_pk_bf16_f32 v4, v12, v13
	v_cvt_pk_bf16_f32 v5, v10, v11
	global_store_dwordx4 v[6:7], v[2:5], off
	s_nop 1
	v_mul_f32_e32 v2, v22, v23
	v_pk_mul_f32 v[4:5], v[40:41], v[2:3] op_sel_hi:[1,0]
	v_pk_mul_f32 v[8:9], v[38:39], v[2:3] op_sel_hi:[1,0]
	v_pk_mul_f32 v[10:11], v[36:37], v[2:3] op_sel_hi:[1,0]
	v_pk_mul_f32 v[12:13], v[34:35], v[2:3] op_sel_hi:[1,0]
	v_cvt_pk_bf16_f32 v2, v8, v9
	v_cvt_pk_bf16_f32 v3, v4, v5
	v_cvt_pk_bf16_f32 v4, v12, v13
	v_cvt_pk_bf16_f32 v5, v10, v11
	global_store_dwordx4 v[6:7], v[2:5], off offset:256
	s_cbranch_vccnz .LBB0_147
	s_andn2_b64 vcc, exec, s[14:15]
	s_cbranch_vccnz .LBB0_146
	s_barrier
	s_branch .LBB0_146

; __device__ __forceinline__ unsigned cvt_pk_bf16(float lo, float hi) { const f32x2 v = {lo, hi}; const bf16x2_t b = __builtin_convertvector(v, bf16x2_t); return __builtin_bit_cast(unsigned, b); }
; #define PG8_SCHED __builtin_amdgcn_sched_barrier(0)
; __device__ __forceinline__ unsigned long long rt() { return __builtin_amdgcn_s_memrealtime(); }
;     __device__ __forceinline__ void operator()(const f32x4 (&acc)[2][2][4][2], const Unit& u, int wr, int wc, int fr, int fq) const {
;         const int row0 = u.pm * BM + wr * 64 + fr, col0 = u.pn * BM + wc * 32 + 8 * fq;
;         const float sc0 = ((smask >> (2 * u.pn)) & 1u) ? sval : 1.0f, sc1 = ((smask >> (2 * u.pn + 1)) & 1u) ? sval : 1.0f;
; #pragma unroll
;         for (int ai = 0; ai < 2; ++ai)
; #pragma unroll
;             for (int m = 0; m < 4; ++m) { bf16_t* rowp = O + (size_t)(row0 + ai * HALF + m * 16) * ldc + col0;
;                 const float rs = rt ? rt[ai * HALF + wr * 64 + m * 16 + fr] : 1.0f;
; #pragma unroll
;                 for (int bj = 0; bj < 2; ++bj) { const float sc = (bj ? sc1 : sc0) * rs; const f32x4 v0 = acc[ai][bj][m][0] * sc, v1 = acc[ai][bj][m][1] * sc;
;                     u32x4 w; w.x = cvt_pk_bf16(v0[0], v0[1]); w.y = cvt_pk_bf16(v0[2], v0[3]); w.z = cvt_pk_bf16(v1[0], v1[1]); w.w = cvt_pk_bf16(v1[2], v1[3]);
;                     *(u32x4*)(rowp + bj * HALF) = w; } }
; template <class Epi, class Sched, bool ALIGN_EPI = false, bool SP2 = false, bool F8 = false>
; __device__ __forceinline__ void gemm_phase(PG8_LAS unsigned char* lds, const Gemm g, const Sched& S, const Epi& E) {
;     ...
;         if constexpr (F8) { asm volatile("s_nop 15\n\ts_nop 15" ::: "memory"); PG8_SCHED; }
.LBB0_165:
	s_nop 7
	s_add_u32 s14, s34, 0x180000
	s_addc_u32 s15, s35, 0
	v_lshl_or_b32 v2, s24, 8, v165
	v_ashrrev_i32_e32 v167, 31, v166
	v_or_b32_e32 v4, s42, v2
	v_lshlrev_b64 v[2:3], 10, v[166:167]
	s_mov_b32 s12, 0x3d800000
	v_lshl_add_u64 v[2:3], s[14:15], 0, v[2:3]
	v_lshlrev_b32_e32 v8, 1, v4
	v_mov_b32_e32 v9, 0
	v_pk_mul_f32 v[6:7], v[160:161], s[12:13] op_sel_hi:[1,0]
	v_pk_mul_f32 v[4:5], v[158:159], s[12:13] op_sel_hi:[1,0]
	v_pk_mul_f32 v[10:11], v[156:157], s[12:13] op_sel_hi:[1,0]
	v_pk_mul_f32 v[12:13], v[154:155], s[12:13] op_sel_hi:[1,0]
	v_lshl_add_u64 v[2:3], v[2:3], 0, v[8:9]
	v_cvt_pk_bf16_f32 v4, v4, v5
	v_cvt_pk_bf16_f32 v5, v6, v7
	v_cvt_pk_bf16_f32 v6, v12, v13
	v_cvt_pk_bf16_f32 v7, v10, v11
	global_store_dwordx4 v[2:3], v[4:7], off
	v_pk_mul_f32 v[10:11], v[140:141], s[12:13] op_sel_hi:[1,0]
	v_pk_mul_f32 v[12:13], v[138:139], s[12:13] op_sel_hi:[1,0]
	v_pk_mul_f32 v[6:7], v[148:149], s[12:13] op_sel_hi:[1,0]
	v_pk_mul_f32 v[4:5], v[146:147], s[12:13] op_sel_hi:[1,0]
	v_pk_mul_f32 v[14:15], v[142:143], s[12:13] op_sel_hi:[1,0]
	v_cvt_pk_bf16_f32 v4, v4, v5
	v_cvt_pk_bf16_f32 v5, v6, v7
	v_cvt_pk_bf16_f32 v6, v12, v13
	v_cvt_pk_bf16_f32 v7, v10, v11
	global_store_dwordx4 v[2:3], v[4:7], off offset:256
	v_pk_mul_f32 v[12:13], v[144:145], s[12:13] op_sel_hi:[1,0]
	s_mov_b32 s0, 0x20000
	v_or_b32_e32 v4, 16, v166
	v_ashrrev_i32_e32 v5, 31, v4
	v_lshlrev_b64 v[4:5], 10, v[4:5]
	v_lshl_add_u64 v[4:5], s[14:15], 0, v[4:5]
	v_lshl_add_u64 v[10:11], v[4:5], 0, v[8:9]
	v_pk_mul_f32 v[6:7], v[152:153], s[12:13] op_sel_hi:[1,0]
	v_pk_mul_f32 v[4:5], v[150:151], s[12:13] op_sel_hi:[1,0]
	s_mov_b64 s[4:5], 0x20000
	v_cvt_pk_bf16_f32 v4, v4, v5
	v_cvt_pk_bf16_f32 v5, v6, v7
	v_cvt_pk_bf16_f32 v6, v14, v15
	v_cvt_pk_bf16_f32 v7, v12, v13
	global_store_dwordx4 v[10:11], v[4:7], off
	v_pk_mul_f32 v[12:13], v[124:125], s[12:13] op_sel_hi:[1,0]
	v_pk_mul_f32 v[14:15], v[122:123], s[12:13] op_sel_hi:[1,0]
	v_pk_mul_f32 v[6:7], v[132:133], s[12:13] op_sel_hi:[1,0]
	v_pk_mul_f32 v[4:5], v[130:131], s[12:13] op_sel_hi:[1,0]
	s_nop 0
	v_cvt_pk_bf16_f32 v4, v4, v5
	v_cvt_pk_bf16_f32 v5, v6, v7
	v_cvt_pk_bf16_f32 v6, v14, v15
	v_cvt_pk_bf16_f32 v7, v12, v13
	global_store_dwordx4 v[10:11], v[4:7], off offset:256
	v_pk_mul_f32 v[12:13], v[128:129], s[12:13] op_sel_hi:[1,0]
	v_pk_mul_f32 v[14:15], v[126:127], s[12:13] op_sel_hi:[1,0]
	v_or_b32_e32 v4, 32, v166
	v_ashrrev_i32_e32 v5, 31, v4
	v_lshlrev_b64 v[4:5], 10, v[4:5]
	v_lshl_add_u64 v[4:5], s[14:15], 0, v[4:5]
	v_lshl_add_u64 v[10:11], v[4:5], 0, v[8:9]
	v_pk_mul_f32 v[6:7], v[136:137], s[12:13] op_sel_hi:[1,0]
	v_pk_mul_f32 v[4:5], v[134:135], s[12:13] op_sel_hi:[1,0]
	s_nop 0
	v_cvt_pk_bf16_f32 v4, v4, v5
	v_cvt_pk_bf16_f32 v5, v6, v7
	v_cvt_pk_bf16_f32 v6, v14, v15
	v_cvt_pk_bf16_f32 v7, v12, v13
	global_store_dwordx4 v[10:11], v[4:7], off
	v_pk_mul_f32 v[12:13], v[108:109], s[12:13] op_sel_hi:[1,0]
	v_pk_mul_f32 v[14:15], v[106:107], s[12:13] op_sel_hi:[1,0]
	v_pk_mul_f32 v[6:7], v[116:117], s[12:13] op_sel_hi:[1,0]
	v_pk_mul_f32 v[4:5], v[114:115], s[12:13] op_sel_hi:[1,0]
	s_nop 0
	v_cvt_pk_bf16_f32 v4, v4, v5
	v_cvt_pk_bf16_f32 v5, v6, v7
	v_cvt_pk_bf16_f32 v6, v14, v15
	v_cvt_pk_bf16_f32 v7, v12, v13
	global_store_dwordx4 v[10:11], v[4:7], off offset:256
	v_pk_mul_f32 v[10:11], v[112:113], s[12:13] op_sel_hi:[1,0]
	v_pk_mul_f32 v[12:13], v[110:111], s[12:13] op_sel_hi:[1,0]
	v_or_b32_e32 v4, 48, v166
	v_ashrrev_i32_e32 v5, 31, v4
	v_lshlrev_b64 v[4:5], 10, v[4:5]
	v_lshl_add_u64 v[4:5], s[14:15], 0, v[4:5]
	v_lshl_add_u64 v[8:9], v[4:5], 0, v[8:9]
	v_pk_mul_f32 v[6:7], v[120:121], s[12:13] op_sel_hi:[1,0]
	v_pk_mul_f32 v[4:5], v[118:119], s[12:13] op_sel_hi:[1,0]
	s_nop 0
	v_cvt_pk_bf16_f32 v4, v4, v5
	v_cvt_pk_bf16_f32 v5, v6, v7
	v_cvt_pk_bf16_f32 v6, v12, v13
	v_cvt_pk_bf16_f32 v7, v10, v11
	global_store_dwordx4 v[8:9], v[4:7], off
	v_pk_mul_f32 v[10:11], v[100:101], s[12:13] op_sel_hi:[1,0]
	v_pk_mul_f32 v[12:13], v[98:99], s[12:13] op_sel_hi:[1,0]
	v_pk_mul_f32 v[6:7], v[104:105], s[12:13] op_sel_hi:[1,0]
	v_pk_mul_f32 v[4:5], v[102:103], s[12:13] op_sel_hi:[1,0]
; __device__ __forceinline__ unsigned cvt_pk_bf16(float lo, float hi) { const f32x2 v = {lo, hi}; const bf16x2_t b = __builtin_convertvector(v, bf16x2_t); return __builtin_bit_cast(unsigned, b); }
; #define PG8_WAIT_V(n) asm volatile("s_waitcnt vmcnt(" #n ")" ::: "memory")
; #define PG8_BAR __builtin_amdgcn_s_barrier()
; __device__ __forceinline__ unsigned long long rt() { return __builtin_amdgcn_s_memrealtime(); }
;     __device__ __forceinline__ void operator()(const f32x4 (&acc)[2][2][4][2], const Unit& u, int wr, int wc, int fr, int fq) const {
;     ...
;             for (int m = 0; m < 4; ++m) { bf16_t* rowp = O + (size_t)(row0 + ai * HALF + m * 16) * ldc + col0;
;                 const float rs = rt ? rt[ai * HALF + wr * 64 + m * 16 + fr] : 1.0f;
; #pragma unroll
;                 for (int bj = 0; bj < 2; ++bj) { const float sc = (bj ? sc1 : sc0) * rs; const f32x4 v0 = acc[ai][bj][m][0] * sc, v1 = acc[ai][bj][m][1] * sc;
;                     u32x4 w; w.x = cvt_pk_bf16(v0[0], v0[1]); w.y = cvt_pk_bf16(v0[2], v0[3]); w.z = cvt_pk_bf16(v1[0], v1[1]); w.w = cvt_pk_bf16(v1[2], v1[3]);
;                     *(u32x4*)(rowp + bj * HALF) = w; } }
; template <class Epi, class Sched, bool ALIGN_EPI = false, bool SP2 = false, bool F8 = false>
; __device__ __forceinline__ void gemm_phase(PG8_LAS unsigned char* lds, const Gemm g, const Sched& S, const Epi& E) {
;     ...
;     PG8_WAIT_V(0);
;     if constexpr (!ALIGN_EPI) { if (wr == 0) PG8_BAR; }
;     PG8_BAR;
	s_nop 0
	v_cvt_pk_bf16_f32 v4, v4, v5
	v_cvt_pk_bf16_f32 v5, v6, v7
	v_cvt_pk_bf16_f32 v6, v12, v13
	v_cvt_pk_bf16_f32 v7, v10, v11
	global_store_dwordx4 v[8:9], v[4:7], off offset:256
	v_pk_mul_f32 v[10:11], v[92:93], s[12:13] op_sel_hi:[1,0]
	v_pk_mul_f32 v[12:13], v[90:91], s[12:13] op_sel_hi:[1,0]
	v_pk_mul_f32 v[6:7], v[96:97], s[12:13] op_sel_hi:[1,0]
	v_pk_mul_f32 v[4:5], v[94:95], s[12:13] op_sel_hi:[1,0]
	v_lshl_add_u64 v[8:9], v[2:3], 0, s[4:5]
	v_cvt_pk_bf16_f32 v4, v4, v5
	v_cvt_pk_bf16_f32 v5, v6, v7
	v_cvt_pk_bf16_f32 v7, v10, v11
	v_add_co_u32_e32 v10, vcc, s0, v2
	v_cvt_pk_bf16_f32 v6, v12, v13
	s_nop 0
	v_addc_co_u32_e32 v11, vcc, 0, v3, vcc
	global_store_dwordx4 v[10:11], v[4:7], off
	v_pk_mul_f32 v[10:11], v[76:77], s[12:13] op_sel_hi:[1,0]
	v_pk_mul_f32 v[12:13], v[74:75], s[12:13] op_sel_hi:[1,0]
	v_pk_mul_f32 v[6:7], v[84:85], s[12:13] op_sel_hi:[1,0]
	v_pk_mul_f32 v[4:5], v[82:83], s[12:13] op_sel_hi:[1,0]
	s_mov_b32 s0, 0x24000
	v_cvt_pk_bf16_f32 v4, v4, v5
	v_cvt_pk_bf16_f32 v5, v6, v7
	v_cvt_pk_bf16_f32 v6, v12, v13
	v_cvt_pk_bf16_f32 v7, v10, v11
	global_store_dwordx4 v[8:9], v[4:7], off offset:256
	v_pk_mul_f32 v[10:11], v[80:81], s[12:13] op_sel_hi:[1,0]
	v_pk_mul_f32 v[12:13], v[78:79], s[12:13] op_sel_hi:[1,0]
	v_pk_mul_f32 v[6:7], v[88:89], s[12:13] op_sel_hi:[1,0]
	v_pk_mul_f32 v[4:5], v[86:87], s[12:13] op_sel_hi:[1,0]
	s_mov_b64 s[4:5], 0x24000
	v_cvt_pk_bf16_f32 v4, v4, v5
	v_cvt_pk_bf16_f32 v5, v6, v7
	v_cvt_pk_bf16_f32 v7, v10, v11
	v_add_co_u32_e32 v10, vcc, s0, v2
	v_cvt_pk_bf16_f32 v6, v12, v13
	s_nop 0
	v_addc_co_u32_e32 v11, vcc, 0, v3, vcc
	global_store_dwordx4 v[10:11], v[4:7], off
	v_pk_mul_f32 v[10:11], v[60:61], s[12:13] op_sel_hi:[1,0]
	v_pk_mul_f32 v[12:13], v[58:59], s[12:13] op_sel_hi:[1,0]
	v_pk_mul_f32 v[6:7], v[68:69], s[12:13] op_sel_hi:[1,0]
	v_pk_mul_f32 v[4:5], v[66:67], s[12:13] op_sel_hi:[1,0]
	v_lshl_add_u64 v[8:9], v[2:3], 0, s[4:5]
	v_cvt_pk_bf16_f32 v4, v4, v5
	v_cvt_pk_bf16_f32 v5, v6, v7
	v_cvt_pk_bf16_f32 v6, v12, v13
	v_cvt_pk_bf16_f32 v7, v10, v11
	global_store_dwordx4 v[8:9], v[4:7], off offset:256
	v_pk_mul_f32 v[10:11], v[64:65], s[12:13] op_sel_hi:[1,0]
	s_mov_b32 s0, 0x28000
	v_pk_mul_f32 v[6:7], v[72:73], s[12:13] op_sel_hi:[1,0]
	v_pk_mul_f32 v[4:5], v[70:71], s[12:13] op_sel_hi:[1,0]
	v_pk_mul_f32 v[12:13], v[62:63], s[12:13] op_sel_hi:[1,0]
	v_cvt_pk_bf16_f32 v4, v4, v5
	v_cvt_pk_bf16_f32 v5, v6, v7
	v_cvt_pk_bf16_f32 v7, v10, v11
	v_add_co_u32_e32 v10, vcc, s0, v2
	v_cvt_pk_bf16_f32 v6, v12, v13
	s_nop 0
	v_addc_co_u32_e32 v11, vcc, 0, v3, vcc
	s_mov_b64 s[4:5], 0x28000
	global_store_dwordx4 v[10:11], v[4:7], off
	v_pk_mul_f32 v[10:11], v[44:45], s[12:13] op_sel_hi:[1,0]
	v_pk_mul_f32 v[12:13], v[42:43], s[12:13] op_sel_hi:[1,0]
	v_pk_mul_f32 v[6:7], v[52:53], s[12:13] op_sel_hi:[1,0]
	v_pk_mul_f32 v[4:5], v[50:51], s[12:13] op_sel_hi:[1,0]
	v_lshl_add_u64 v[8:9], v[2:3], 0, s[4:5]
	v_cvt_pk_bf16_f32 v4, v4, v5
	v_cvt_pk_bf16_f32 v5, v6, v7
	v_cvt_pk_bf16_f32 v6, v12, v13
	v_cvt_pk_bf16_f32 v7, v10, v11
	s_mov_b64 s[4:5], 0x2c000
	s_mov_b32 s0, 0x2c000
	global_store_dwordx4 v[8:9], v[4:7], off offset:256
	v_lshl_add_u64 v[8:9], v[2:3], 0, s[4:5]
	v_pk_mul_f32 v[10:11], v[48:49], s[12:13] op_sel_hi:[1,0]
	v_pk_mul_f32 v[6:7], v[56:57], s[12:13] op_sel_hi:[1,0]
	v_pk_mul_f32 v[4:5], v[54:55], s[12:13] op_sel_hi:[1,0]
	v_pk_mul_f32 v[12:13], v[46:47], s[12:13] op_sel_hi:[1,0]
	v_add_co_u32_e32 v2, vcc, s0, v2
	v_cvt_pk_bf16_f32 v4, v4, v5
	v_cvt_pk_bf16_f32 v5, v6, v7
	v_cvt_pk_bf16_f32 v6, v12, v13
	v_cvt_pk_bf16_f32 v7, v10, v11
	v_addc_co_u32_e32 v3, vcc, 0, v3, vcc
	global_store_dwordx4 v[2:3], v[4:7], off
	v_pk_mul_f32 v[2:3], v[38:39], s[12:13] op_sel_hi:[1,0]
	v_pk_mul_f32 v[10:11], v[34:35], s[12:13] op_sel_hi:[1,0]
	v_pk_mul_f32 v[4:5], v[40:41], s[12:13] op_sel_hi:[1,0]
	v_pk_mul_f32 v[6:7], v[36:37], s[12:13] op_sel_hi:[1,0]
	v_cvt_pk_bf16_f32 v2, v2, v3
	v_cvt_pk_bf16_f32 v3, v4, v5
	v_cvt_pk_bf16_f32 v4, v10, v11
	v_cvt_pk_bf16_f32 v5, v6, v7
	global_store_dwordx4 v[8:9], v[2:5], off offset:256
	s_waitcnt vmcnt(0)
	s_barrier

; __device__ __forceinline__ unsigned cvt_pk_bf16(float lo, float hi) { const f32x2 v = {lo, hi}; const bf16x2_t b = __builtin_convertvector(v, bf16x2_t); return __builtin_bit_cast(unsigned, b); }
; #define PG8_SCHED __builtin_amdgcn_sched_barrier(0)
; __device__ __forceinline__ unsigned long long rt() { return __builtin_amdgcn_s_memrealtime(); }
;     __device__ __forceinline__ void operator()(const f32x4 (&acc)[2][2][4][2], const Unit& u, int wr, int wc, int fr, int fq) const {
;         const int row0 = u.pm * BM + wr * 64 + fr, col0 = u.pn * BM + wc * 32 + 8 * fq;
;         const float sc0 = ((smask >> (2 * u.pn)) & 1u) ? sval : 1.0f, sc1 = ((smask >> (2 * u.pn + 1)) & 1u) ? sval : 1.0f;
; #pragma unroll
;         for (int ai = 0; ai < 2; ++ai)
; #pragma unroll
;             for (int m = 0; m < 4; ++m) { bf16_t* rowp = O + (size_t)(row0 + ai * HALF + m * 16) * ldc + col0;
;                 const float rs = rt ? rt[ai * HALF + wr * 64 + m * 16 + fr] : 1.0f;
; #pragma unroll
;                 for (int bj = 0; bj < 2; ++bj) { const float sc = (bj ? sc1 : sc0) * rs; const f32x4 v0 = acc[ai][bj][m][0] * sc, v1 = acc[ai][bj][m][1] * sc;
;                     u32x4 w; w.x = cvt_pk_bf16(v0[0], v0[1]); w.y = cvt_pk_bf16(v0[2], v0[3]); w.z = cvt_pk_bf16(v1[0], v1[1]); w.w = cvt_pk_bf16(v1[2], v1[3]);
;                     *(u32x4*)(rowp + bj * HALF) = w; } }
; template <class Epi, class Sched, bool ALIGN_EPI = false, bool SP2 = false, bool F8 = false>
; __device__ __forceinline__ void gemm_phase(PG8_LAS unsigned char* lds, const Gemm g, const Sched& S, const Epi& E) {
;     ...
;         if constexpr (F8) { asm volatile("s_nop 15\n\ts_nop 15" ::: "memory"); PG8_SCHED; }
.LBB0_173:
	s_nop 7
	s_add_u32 s12, s34, 0x1c0000
	s_addc_u32 s13, s35, 0
	v_lshl_or_b32 v2, s24, 8, v165
	v_ashrrev_i32_e32 v167, 31, v166
	v_or_b32_e32 v4, s42, v2
	v_lshlrev_b64 v[2:3], 10, v[166:167]
	s_mov_b32 s8, 0x3d800000
	v_lshl_add_u64 v[2:3], s[12:13], 0, v[2:3]
	v_lshlrev_b32_e32 v8, 1, v4
	v_mov_b32_e32 v9, 0
	v_pk_mul_f32 v[6:7], v[160:161], s[8:9] op_sel_hi:[1,0]
	v_pk_mul_f32 v[4:5], v[158:159], s[8:9] op_sel_hi:[1,0]
	v_pk_mul_f32 v[10:11], v[156:157], s[8:9] op_sel_hi:[1,0]
	v_pk_mul_f32 v[12:13], v[154:155], s[8:9] op_sel_hi:[1,0]
	v_lshl_add_u64 v[2:3], v[2:3], 0, v[8:9]
	v_cvt_pk_bf16_f32 v4, v4, v5
	v_cvt_pk_bf16_f32 v5, v6, v7
	v_cvt_pk_bf16_f32 v6, v12, v13
	v_cvt_pk_bf16_f32 v7, v10, v11
	global_store_dwordx4 v[2:3], v[4:7], off
	v_pk_mul_f32 v[10:11], v[140:141], s[8:9] op_sel_hi:[1,0]
	v_pk_mul_f32 v[12:13], v[138:139], s[8:9] op_sel_hi:[1,0]
	v_pk_mul_f32 v[6:7], v[148:149], s[8:9] op_sel_hi:[1,0]
	v_pk_mul_f32 v[4:5], v[146:147], s[8:9] op_sel_hi:[1,0]
	v_pk_mul_f32 v[14:15], v[142:143], s[8:9] op_sel_hi:[1,0]
	v_cvt_pk_bf16_f32 v4, v4, v5
	v_cvt_pk_bf16_f32 v5, v6, v7
	v_cvt_pk_bf16_f32 v6, v12, v13
	v_cvt_pk_bf16_f32 v7, v10, v11
	global_store_dwordx4 v[2:3], v[4:7], off offset:256
	v_pk_mul_f32 v[12:13], v[144:145], s[8:9] op_sel_hi:[1,0]
	s_mov_b32 s0, 0x20000
	v_or_b32_e32 v4, 16, v166
	v_ashrrev_i32_e32 v5, 31, v4
	v_lshlrev_b64 v[4:5], 10, v[4:5]
	v_lshl_add_u64 v[4:5], s[12:13], 0, v[4:5]
	v_lshl_add_u64 v[10:11], v[4:5], 0, v[8:9]
	v_pk_mul_f32 v[6:7], v[152:153], s[8:9] op_sel_hi:[1,0]
	v_pk_mul_f32 v[4:5], v[150:151], s[8:9] op_sel_hi:[1,0]
	s_mov_b64 s[4:5], 0x20000
	v_cvt_pk_bf16_f32 v4, v4, v5
	v_cvt_pk_bf16_f32 v5, v6, v7
	v_cvt_pk_bf16_f32 v6, v14, v15
	v_cvt_pk_bf16_f32 v7, v12, v13
	global_store_dwordx4 v[10:11], v[4:7], off
	v_pk_mul_f32 v[12:13], v[124:125], s[8:9] op_sel_hi:[1,0]
	v_pk_mul_f32 v[14:15], v[122:123], s[8:9] op_sel_hi:[1,0]
	v_pk_mul_f32 v[6:7], v[132:133], s[8:9] op_sel_hi:[1,0]
	v_pk_mul_f32 v[4:5], v[130:131], s[8:9] op_sel_hi:[1,0]
	s_nop 0
	v_cvt_pk_bf16_f32 v4, v4, v5
	v_cvt_pk_bf16_f32 v5, v6, v7
	v_cvt_pk_bf16_f32 v6, v14, v15
	v_cvt_pk_bf16_f32 v7, v12, v13
	global_store_dwordx4 v[10:11], v[4:7], off offset:256
	v_pk_mul_f32 v[12:13], v[128:129], s[8:9] op_sel_hi:[1,0]
	v_pk_mul_f32 v[14:15], v[126:127], s[8:9] op_sel_hi:[1,0]
	v_or_b32_e32 v4, 32, v166
	v_ashrrev_i32_e32 v5, 31, v4
	v_lshlrev_b64 v[4:5], 10, v[4:5]
	v_lshl_add_u64 v[4:5], s[12:13], 0, v[4:5]
	v_lshl_add_u64 v[10:11], v[4:5], 0, v[8:9]
	v_pk_mul_f32 v[6:7], v[136:137], s[8:9] op_sel_hi:[1,0]
	v_pk_mul_f32 v[4:5], v[134:135], s[8:9] op_sel_hi:[1,0]
	s_nop 0
	v_cvt_pk_bf16_f32 v4, v4, v5
	v_cvt_pk_bf16_f32 v5, v6, v7
	v_cvt_pk_bf16_f32 v6, v14, v15
	v_cvt_pk_bf16_f32 v7, v12, v13
	global_store_dwordx4 v[10:11], v[4:7], off
	v_pk_mul_f32 v[12:13], v[108:109], s[8:9] op_sel_hi:[1,0]
	v_pk_mul_f32 v[14:15], v[106:107], s[8:9] op_sel_hi:[1,0]
	v_pk_mul_f32 v[6:7], v[116:117], s[8:9] op_sel_hi:[1,0]
	v_pk_mul_f32 v[4:5], v[114:115], s[8:9] op_sel_hi:[1,0]
	s_nop 0
	v_cvt_pk_bf16_f32 v4, v4, v5
	v_cvt_pk_bf16_f32 v5, v6, v7
	v_cvt_pk_bf16_f32 v6, v14, v15
	v_cvt_pk_bf16_f32 v7, v12, v13
	global_store_dwordx4 v[10:11], v[4:7], off offset:256
	v_pk_mul_f32 v[10:11], v[112:113], s[8:9] op_sel_hi:[1,0]
	v_pk_mul_f32 v[12:13], v[110:111], s[8:9] op_sel_hi:[1,0]
	v_or_b32_e32 v4, 48, v166
	v_ashrrev_i32_e32 v5, 31, v4
	v_lshlrev_b64 v[4:5], 10, v[4:5]
	v_lshl_add_u64 v[4:5], s[12:13], 0, v[4:5]
	v_lshl_add_u64 v[8:9], v[4:5], 0, v[8:9]
	v_pk_mul_f32 v[6:7], v[120:121], s[8:9] op_sel_hi:[1,0]
	v_pk_mul_f32 v[4:5], v[118:119], s[8:9] op_sel_hi:[1,0]
	s_nop 0
	v_cvt_pk_bf16_f32 v4, v4, v5
	v_cvt_pk_bf16_f32 v5, v6, v7
	v_cvt_pk_bf16_f32 v6, v12, v13
	v_cvt_pk_bf16_f32 v7, v10, v11
	global_store_dwordx4 v[8:9], v[4:7], off
	v_pk_mul_f32 v[10:11], v[100:101], s[8:9] op_sel_hi:[1,0]
	v_pk_mul_f32 v[12:13], v[98:99], s[8:9] op_sel_hi:[1,0]
	v_pk_mul_f32 v[6:7], v[104:105], s[8:9] op_sel_hi:[1,0]
	v_pk_mul_f32 v[4:5], v[102:103], s[8:9] op_sel_hi:[1,0]
; __device__ __forceinline__ unsigned cvt_pk_bf16(float lo, float hi) { const f32x2 v = {lo, hi}; const bf16x2_t b = __builtin_convertvector(v, bf16x2_t); return __builtin_bit_cast(unsigned, b); }
; #define PG8_WAIT_V(n) asm volatile("s_waitcnt vmcnt(" #n ")" ::: "memory")
; #define PG8_BAR __builtin_amdgcn_s_barrier()
; __device__ __forceinline__ unsigned long long rt() { return __builtin_amdgcn_s_memrealtime(); }
;     __device__ __forceinline__ void operator()(const f32x4 (&acc)[2][2][4][2], const Unit& u, int wr, int wc, int fr, int fq) const {
;     ...
;             for (int m = 0; m < 4; ++m) { bf16_t* rowp = O + (size_t)(row0 + ai * HALF + m * 16) * ldc + col0;
;                 const float rs = rt ? rt[ai * HALF + wr * 64 + m * 16 + fr] : 1.0f;
; #pragma unroll
;                 for (int bj = 0; bj < 2; ++bj) { const float sc = (bj ? sc1 : sc0) * rs; const f32x4 v0 = acc[ai][bj][m][0] * sc, v1 = acc[ai][bj][m][1] * sc;
;                     u32x4 w; w.x = cvt_pk_bf16(v0[0], v0[1]); w.y = cvt_pk_bf16(v0[2], v0[3]); w.z = cvt_pk_bf16(v1[0], v1[1]); w.w = cvt_pk_bf16(v1[2], v1[3]);
;                     *(u32x4*)(rowp + bj * HALF) = w; } }
; template <class Epi, class Sched, bool ALIGN_EPI = false, bool SP2 = false, bool F8 = false>
; __device__ __forceinline__ void gemm_phase(PG8_LAS unsigned char* lds, const Gemm g, const Sched& S, const Epi& E) {
;     ...
;     PG8_WAIT_V(0);
;     if constexpr (!ALIGN_EPI) { if (wr == 0) PG8_BAR; }
;     PG8_BAR;
	s_nop 0
	v_cvt_pk_bf16_f32 v4, v4, v5
	v_cvt_pk_bf16_f32 v5, v6, v7
	v_cvt_pk_bf16_f32 v6, v12, v13
	v_cvt_pk_bf16_f32 v7, v10, v11
	global_store_dwordx4 v[8:9], v[4:7], off offset:256
	v_pk_mul_f32 v[10:11], v[92:93], s[8:9] op_sel_hi:[1,0]
	v_pk_mul_f32 v[12:13], v[90:91], s[8:9] op_sel_hi:[1,0]
	v_pk_mul_f32 v[6:7], v[96:97], s[8:9] op_sel_hi:[1,0]
	v_pk_mul_f32 v[4:5], v[94:95], s[8:9] op_sel_hi:[1,0]
	v_lshl_add_u64 v[8:9], v[2:3], 0, s[4:5]
	v_cvt_pk_bf16_f32 v4, v4, v5
	v_cvt_pk_bf16_f32 v5, v6, v7
	v_cvt_pk_bf16_f32 v7, v10, v11
	v_add_co_u32_e32 v10, vcc, s0, v2
	v_cvt_pk_bf16_f32 v6, v12, v13
	s_nop 0
	v_addc_co_u32_e32 v11, vcc, 0, v3, vcc
	global_store_dwordx4 v[10:11], v[4:7], off
	v_pk_mul_f32 v[10:11], v[76:77], s[8:9] op_sel_hi:[1,0]
	v_pk_mul_f32 v[12:13], v[74:75], s[8:9] op_sel_hi:[1,0]
	v_pk_mul_f32 v[6:7], v[84:85], s[8:9] op_sel_hi:[1,0]
	v_pk_mul_f32 v[4:5], v[82:83], s[8:9] op_sel_hi:[1,0]
	s_mov_b32 s0, 0x24000
	v_cvt_pk_bf16_f32 v4, v4, v5
	v_cvt_pk_bf16_f32 v5, v6, v7
	v_cvt_pk_bf16_f32 v6, v12, v13
	v_cvt_pk_bf16_f32 v7, v10, v11
	global_store_dwordx4 v[8:9], v[4:7], off offset:256
	v_pk_mul_f32 v[10:11], v[80:81], s[8:9] op_sel_hi:[1,0]
	v_pk_mul_f32 v[12:13], v[78:79], s[8:9] op_sel_hi:[1,0]
	v_pk_mul_f32 v[6:7], v[88:89], s[8:9] op_sel_hi:[1,0]
	v_pk_mul_f32 v[4:5], v[86:87], s[8:9] op_sel_hi:[1,0]
	s_mov_b64 s[4:5], 0x24000
	v_cvt_pk_bf16_f32 v4, v4, v5
	v_cvt_pk_bf16_f32 v5, v6, v7
	v_cvt_pk_bf16_f32 v7, v10, v11
	v_add_co_u32_e32 v10, vcc, s0, v2
	v_cvt_pk_bf16_f32 v6, v12, v13
	s_nop 0
	v_addc_co_u32_e32 v11, vcc, 0, v3, vcc
	global_store_dwordx4 v[10:11], v[4:7], off
	v_pk_mul_f32 v[10:11], v[60:61], s[8:9] op_sel_hi:[1,0]
	v_pk_mul_f32 v[12:13], v[58:59], s[8:9] op_sel_hi:[1,0]
	v_pk_mul_f32 v[6:7], v[68:69], s[8:9] op_sel_hi:[1,0]
	v_pk_mul_f32 v[4:5], v[66:67], s[8:9] op_sel_hi:[1,0]
	v_lshl_add_u64 v[8:9], v[2:3], 0, s[4:5]
	v_cvt_pk_bf16_f32 v4, v4, v5
	v_cvt_pk_bf16_f32 v5, v6, v7
	v_cvt_pk_bf16_f32 v6, v12, v13
	v_cvt_pk_bf16_f32 v7, v10, v11
	global_store_dwordx4 v[8:9], v[4:7], off offset:256
	v_pk_mul_f32 v[10:11], v[64:65], s[8:9] op_sel_hi:[1,0]
	s_mov_b32 s0, 0x28000
	v_pk_mul_f32 v[6:7], v[72:73], s[8:9] op_sel_hi:[1,0]
	v_pk_mul_f32 v[4:5], v[70:71], s[8:9] op_sel_hi:[1,0]
	v_pk_mul_f32 v[12:13], v[62:63], s[8:9] op_sel_hi:[1,0]
	v_cvt_pk_bf16_f32 v4, v4, v5
	v_cvt_pk_bf16_f32 v5, v6, v7
	v_cvt_pk_bf16_f32 v7, v10, v11
	v_add_co_u32_e32 v10, vcc, s0, v2
	v_cvt_pk_bf16_f32 v6, v12, v13
	s_nop 0
	v_addc_co_u32_e32 v11, vcc, 0, v3, vcc
	s_mov_b64 s[4:5], 0x28000
	global_store_dwordx4 v[10:11], v[4:7], off
	v_pk_mul_f32 v[10:11], v[44:45], s[8:9] op_sel_hi:[1,0]
	v_pk_mul_f32 v[12:13], v[42:43], s[8:9] op_sel_hi:[1,0]
	v_pk_mul_f32 v[6:7], v[52:53], s[8:9] op_sel_hi:[1,0]
	v_pk_mul_f32 v[4:5], v[50:51], s[8:9] op_sel_hi:[1,0]
	v_lshl_add_u64 v[8:9], v[2:3], 0, s[4:5]
	v_cvt_pk_bf16_f32 v4, v4, v5
	v_cvt_pk_bf16_f32 v5, v6, v7
	v_cvt_pk_bf16_f32 v6, v12, v13
	v_cvt_pk_bf16_f32 v7, v10, v11
	s_mov_b64 s[4:5], 0x2c000
	s_mov_b32 s0, 0x2c000
	global_store_dwordx4 v[8:9], v[4:7], off offset:256
	v_lshl_add_u64 v[8:9], v[2:3], 0, s[4:5]
	v_pk_mul_f32 v[10:11], v[48:49], s[8:9] op_sel_hi:[1,0]
	v_pk_mul_f32 v[6:7], v[56:57], s[8:9] op_sel_hi:[1,0]
	v_pk_mul_f32 v[4:5], v[54:55], s[8:9] op_sel_hi:[1,0]
	v_pk_mul_f32 v[12:13], v[46:47], s[8:9] op_sel_hi:[1,0]
	v_add_co_u32_e32 v2, vcc, s0, v2
	v_cvt_pk_bf16_f32 v4, v4, v5
	v_cvt_pk_bf16_f32 v5, v6, v7
	v_cvt_pk_bf16_f32 v6, v12, v13
	v_cvt_pk_bf16_f32 v7, v10, v11
	v_addc_co_u32_e32 v3, vcc, 0, v3, vcc
	global_store_dwordx4 v[2:3], v[4:7], off
	v_pk_mul_f32 v[2:3], v[38:39], s[8:9] op_sel_hi:[1,0]
	v_pk_mul_f32 v[10:11], v[34:35], s[8:9] op_sel_hi:[1,0]
	v_pk_mul_f32 v[4:5], v[40:41], s[8:9] op_sel_hi:[1,0]
	v_pk_mul_f32 v[6:7], v[36:37], s[8:9] op_sel_hi:[1,0]
	v_cvt_pk_bf16_f32 v2, v2, v3
	v_cvt_pk_bf16_f32 v3, v4, v5
	v_cvt_pk_bf16_f32 v4, v10, v11
	v_cvt_pk_bf16_f32 v5, v6, v7
	global_store_dwordx4 v[8:9], v[2:5], off offset:256
	s_waitcnt vmcnt(0)
	s_barrier

; __device__ __forceinline__ unsigned cvt_pk_bf16(float lo, float hi) { const f32x2 v = {lo, hi}; const bf16x2_t b = __builtin_convertvector(v, bf16x2_t); return __builtin_bit_cast(unsigned, b); }
; #define PG8_SCHED __builtin_amdgcn_sched_barrier(0)
; __device__ __forceinline__ unsigned long long rt() { return __builtin_amdgcn_s_memrealtime(); }
;     __device__ __forceinline__ void operator()(const f32x4 (&acc)[2][2][4][2], const Unit& u, int wr, int wc, int fr, int fq) const {
;         const int row0 = u.pm * BM + wr * 64 + fr, col0 = u.pn * BM + wc * 32 + 8 * fq;
;         const float sc0 = ((smask >> (2 * u.pn)) & 1u) ? sval : 1.0f, sc1 = ((smask >> (2 * u.pn + 1)) & 1u) ? sval : 1.0f;
; #pragma unroll
;         for (int ai = 0; ai < 2; ++ai)
; #pragma unroll
;             for (int m = 0; m < 4; ++m) { bf16_t* rowp = O + (size_t)(row0 + ai * HALF + m * 16) * ldc + col0;
;                 const float rs = rt ? rt[ai * HALF + wr * 64 + m * 16 + fr] : 1.0f;
; #pragma unroll
;                 for (int bj = 0; bj < 2; ++bj) { const float sc = (bj ? sc1 : sc0) * rs; const f32x4 v0 = acc[ai][bj][m][0] * sc, v1 = acc[ai][bj][m][1] * sc;
;                     u32x4 w; w.x = cvt_pk_bf16(v0[0], v0[1]); w.y = cvt_pk_bf16(v0[2], v0[3]); w.z = cvt_pk_bf16(v1[0], v1[1]); w.w = cvt_pk_bf16(v1[2], v1[3]);
;                     *(u32x4*)(rowp + bj * HALF) = w; } }
; template <class Epi, class Sched, bool ALIGN_EPI = false, bool SP2 = false, bool F8 = false>
; __device__ __forceinline__ void gemm_phase(PG8_LAS unsigned char* lds, const Gemm g, const Sched& S, const Epi& E) {
;     ...
;         if constexpr (F8) { asm volatile("s_nop 15\n\ts_nop 15" ::: "memory"); PG8_SCHED; }
.LBB0_805:
	s_nop 7
	s_lshl_b32 s0, s82, 1
	s_lshl_b32 s1, 1, s0
	s_and_b32 s1, s1, 0x41041
	s_cmp_eq_u32 s1, 0
	s_cselect_b64 s[4:5], -1, 0
	s_lshl_b32 s0, 2, s0
	ds_read2_b32 v[10:11], v191 offset1:16
	s_and_b32 s0, s0, 0x82082
	v_lshl_or_b32 v4, s82, 8, v193
	s_cmp_eq_u32 s0, 0
	v_lshl_add_u32 v20, s40, 8, v165
	v_cndmask_b32_e64 v21, v198, 1.0, s[4:5]
	s_cselect_b64 s[4:5], -1, 0
	v_ashrrev_i32_e32 v5, 31, v4
	v_mov_b64_e32 v[2:3], s[16:17]
	v_cndmask_b32_e64 v22, v198, 1.0, s[4:5]
	v_mad_i64_i32 v[6:7], s[4:5], v20, s81, v[2:3]
	v_lshlrev_b64 v[4:5], 1, v[4:5]
	v_lshl_add_u64 v[12:13], v[6:7], 0, v[4:5]
	s_waitcnt lgkmcnt(0)
	v_mul_f32_e32 v6, v21, v10
	v_pk_mul_f32 v[8:9], v[160:161], v[6:7] op_sel_hi:[1,0]
	v_pk_mul_f32 v[14:15], v[158:159], v[6:7] op_sel_hi:[1,0]
	v_pk_mul_f32 v[16:17], v[156:157], v[6:7] op_sel_hi:[1,0]
	v_pk_mul_f32 v[18:19], v[154:155], v[6:7] op_sel_hi:[1,0]
	v_cvt_pk_bf16_f32 v6, v14, v15
	v_cvt_pk_bf16_f32 v7, v8, v9
	v_cvt_pk_bf16_f32 v8, v18, v19
	v_cvt_pk_bf16_f32 v9, v16, v17
	global_store_dwordx4 v[12:13], v[6:9], off
	s_andn2_b64 vcc, exec, s[8:9]
	s_mov_b64 s[8:9], -1
	v_mul_f32_e32 v6, v22, v10
	v_pk_mul_f32 v[8:9], v[148:149], v[6:7] op_sel_hi:[1,0]
	v_pk_mul_f32 v[14:15], v[146:147], v[6:7] op_sel_hi:[1,0]
	v_pk_mul_f32 v[16:17], v[140:141], v[6:7] op_sel_hi:[1,0]
	v_pk_mul_f32 v[18:19], v[138:139], v[6:7] op_sel_hi:[1,0]
	v_cvt_pk_bf16_f32 v6, v14, v15
	v_cvt_pk_bf16_f32 v7, v8, v9
	v_cvt_pk_bf16_f32 v8, v18, v19
	v_cvt_pk_bf16_f32 v9, v16, v17
	global_store_dwordx4 v[12:13], v[6:9], off offset:256
	ds_read_b32 v23, v191 offset:704
	s_nop 0
	v_or_b32_e32 v6, 16, v20
	v_mad_i64_i32 v[6:7], s[4:5], v6, s81, v[2:3]
	v_lshl_add_u64 v[12:13], v[6:7], 0, v[4:5]
	v_mul_f32_e32 v6, v21, v11
	v_pk_mul_f32 v[8:9], v[152:153], v[6:7] op_sel_hi:[1,0]
	v_pk_mul_f32 v[14:15], v[150:151], v[6:7] op_sel_hi:[1,0]
	v_pk_mul_f32 v[16:17], v[144:145], v[6:7] op_sel_hi:[1,0]
	v_pk_mul_f32 v[18:19], v[142:143], v[6:7] op_sel_hi:[1,0]
	v_cvt_pk_bf16_f32 v6, v14, v15
	v_cvt_pk_bf16_f32 v7, v8, v9
	v_cvt_pk_bf16_f32 v8, v18, v19
	v_cvt_pk_bf16_f32 v9, v16, v17
	global_store_dwordx4 v[12:13], v[6:9], off
	s_nop 1
	v_mul_f32_e32 v6, v22, v11
	v_pk_mul_f32 v[10:11], v[134:135], v[6:7] op_sel_hi:[1,0]
	v_pk_mul_f32 v[8:9], v[136:137], v[6:7] op_sel_hi:[1,0]
	v_pk_mul_f32 v[14:15], v[128:129], v[6:7] op_sel_hi:[1,0]
	v_pk_mul_f32 v[16:17], v[126:127], v[6:7] op_sel_hi:[1,0]
	v_cvt_pk_bf16_f32 v6, v10, v11
	ds_read2_b32 v[10:11], v191 offset0:32 offset1:48
	v_cvt_pk_bf16_f32 v7, v8, v9
	v_cvt_pk_bf16_f32 v8, v16, v17
	v_cvt_pk_bf16_f32 v9, v14, v15
	global_store_dwordx4 v[12:13], v[6:9], off offset:256
	s_nop 1
	v_or_b32_e32 v6, 32, v20
	v_mad_i64_i32 v[6:7], s[4:5], v6, s81, v[2:3]
	v_lshl_add_u64 v[12:13], v[6:7], 0, v[4:5]
	s_waitcnt lgkmcnt(0)
	v_mul_f32_e32 v6, v21, v10
	v_pk_mul_f32 v[8:9], v[132:133], v[6:7] op_sel_hi:[1,0]
	v_pk_mul_f32 v[14:15], v[130:131], v[6:7] op_sel_hi:[1,0]
	v_pk_mul_f32 v[16:17], v[124:125], v[6:7] op_sel_hi:[1,0]
	v_pk_mul_f32 v[18:19], v[122:123], v[6:7] op_sel_hi:[1,0]
	v_cvt_pk_bf16_f32 v6, v14, v15
	v_cvt_pk_bf16_f32 v7, v8, v9
	v_cvt_pk_bf16_f32 v8, v18, v19
	v_cvt_pk_bf16_f32 v9, v16, v17
	global_store_dwordx4 v[12:13], v[6:9], off
	s_nop 1
	v_mul_f32_e32 v6, v22, v10
	v_pk_mul_f32 v[8:9], v[116:117], v[6:7] op_sel_hi:[1,0]
	v_pk_mul_f32 v[14:15], v[114:115], v[6:7] op_sel_hi:[1,0]
	v_pk_mul_f32 v[16:17], v[108:109], v[6:7] op_sel_hi:[1,0]
	v_pk_mul_f32 v[18:19], v[106:107], v[6:7] op_sel_hi:[1,0]
	v_cvt_pk_bf16_f32 v6, v14, v15
	v_cvt_pk_bf16_f32 v7, v8, v9
	v_cvt_pk_bf16_f32 v8, v18, v19
	v_cvt_pk_bf16_f32 v9, v16, v17
	global_store_dwordx4 v[12:13], v[6:9], off offset:256
	s_nop 1
	v_or_b32_e32 v6, 48, v20
	v_mad_i64_i32 v[6:7], s[4:5], v6, s81, v[2:3]
	v_lshl_add_u64 v[12:13], v[6:7], 0, v[4:5]
	v_mul_f32_e32 v6, v21, v11
	v_pk_mul_f32 v[8:9], v[120:121], v[6:7] op_sel_hi:[1,0]
	v_pk_mul_f32 v[14:15], v[118:119], v[6:7] op_sel_hi:[1,0]
	v_pk_mul_f32 v[16:17], v[112:113], v[6:7] op_sel_hi:[1,0]
	v_pk_mul_f32 v[18:19], v[110:111], v[6:7] op_sel_hi:[1,0]
	v_cvt_pk_bf16_f32 v6, v14, v15
	v_cvt_pk_bf16_f32 v7, v8, v9
	v_cvt_pk_bf16_f32 v8, v18, v19
	v_cvt_pk_bf16_f32 v9, v16, v17
	global_store_dwordx4 v[12:13], v[6:9], off
	ds_read_b32 v18, v192
	s_nop 0
	v_mul_f32_e32 v6, v22, v11
	v_pk_mul_f32 v[8:9], v[104:105], v[6:7] op_sel_hi:[1,0]
	v_pk_mul_f32 v[10:11], v[102:103], v[6:7] op_sel_hi:[1,0]
	v_pk_mul_f32 v[14:15], v[100:101], v[6:7] op_sel_hi:[1,0]
	v_pk_mul_f32 v[16:17], v[98:99], v[6:7] op_sel_hi:[1,0]
	v_cvt_pk_bf16_f32 v6, v10, v11
	v_cvt_pk_bf16_f32 v7, v8, v9
	v_cvt_pk_bf16_f32 v8, v16, v17
	v_cvt_pk_bf16_f32 v9, v14, v15
	global_store_dwordx4 v[12:13], v[6:9], off offset:256
	s_nop 1
	v_add_u32_e32 v6, 0x80, v20
	v_mad_i64_i32 v[6:7], s[4:5], v6, s81, v[2:3]
	v_lshl_add_u64 v[10:11], v[6:7], 0, v[4:5]
	s_waitcnt lgkmcnt(0)
; __device__ __forceinline__ unsigned cvt_pk_bf16(float lo, float hi) { const f32x2 v = {lo, hi}; const bf16x2_t b = __builtin_convertvector(v, bf16x2_t); return __builtin_bit_cast(unsigned, b); }
; #define PG8_BAR __builtin_amdgcn_s_barrier()
; __device__ __forceinline__ unsigned long long rt() { return __builtin_amdgcn_s_memrealtime(); }
;     __device__ __forceinline__ void operator()(const f32x4 (&acc)[2][2][4][2], const Unit& u, int wr, int wc, int fr, int fq) const {
;     ...
;             for (int m = 0; m < 4; ++m) { bf16_t* rowp = O + (size_t)(row0 + ai * HALF + m * 16) * ldc + col0;
;                 const float rs = rt ? rt[ai * HALF + wr * 64 + m * 16 + fr] : 1.0f;
; #pragma unroll
;                 for (int bj = 0; bj < 2; ++bj) { const float sc = (bj ? sc1 : sc0) * rs; const f32x4 v0 = acc[ai][bj][m][0] * sc, v1 = acc[ai][bj][m][1] * sc;
;                     u32x4 w; w.x = cvt_pk_bf16(v0[0], v0[1]); w.y = cvt_pk_bf16(v0[2], v0[3]); w.z = cvt_pk_bf16(v1[0], v1[1]); w.w = cvt_pk_bf16(v1[2], v1[3]);
;                     *(u32x4*)(rowp + bj * HALF) = w; } }
; template <class Epi, class Sched, bool ALIGN_EPI = false, bool SP2 = false, bool F8 = false>
; __device__ __forceinline__ void gemm_phase(PG8_LAS unsigned char* lds, const Gemm g, const Sched& S, const Epi& E) {
;     ...
;         if (!has_next) break;
; #pragma unroll
;         for (int a = 0; a < 2; ++a)
; #pragma unroll
;             for (int b = 0; b < 2; ++b)
; #pragma unroll
;                 for (int m = 0; m < 4; ++m)
; #pragma unroll
;                     for (int n = 0; n < 2; ++n) acc[a][b][m][n] = (f32x4){0.f, 0.f, 0.f, 0.f};
;         cur = nxt; cA = nA; cB = nB; ++ui;
;         if constexpr (ALIGN_EPI) { if (wr == 1) PG8_BAR; }
	v_mul_f32_e32 v6, v21, v18
	v_pk_mul_f32 v[8:9], v[96:97], v[6:7] op_sel_hi:[1,0]
	v_pk_mul_f32 v[12:13], v[94:95], v[6:7] op_sel_hi:[1,0]
	v_pk_mul_f32 v[14:15], v[92:93], v[6:7] op_sel_hi:[1,0]
	v_pk_mul_f32 v[16:17], v[90:91], v[6:7] op_sel_hi:[1,0]
	v_cvt_pk_bf16_f32 v6, v12, v13
	v_cvt_pk_bf16_f32 v7, v8, v9
	v_cvt_pk_bf16_f32 v8, v16, v17
	v_cvt_pk_bf16_f32 v9, v14, v15
	global_store_dwordx4 v[10:11], v[6:9], off
	s_nop 1
	v_mul_f32_e32 v6, v22, v18
	v_pk_mul_f32 v[8:9], v[80:81], v[6:7] op_sel_hi:[1,0]
	v_pk_mul_f32 v[12:13], v[78:79], v[6:7] op_sel_hi:[1,0]
	v_pk_mul_f32 v[14:15], v[76:77], v[6:7] op_sel_hi:[1,0]
	v_pk_mul_f32 v[16:17], v[74:75], v[6:7] op_sel_hi:[1,0]
	v_cvt_pk_bf16_f32 v6, v12, v13
	v_cvt_pk_bf16_f32 v7, v8, v9
	v_cvt_pk_bf16_f32 v8, v16, v17
	v_cvt_pk_bf16_f32 v9, v14, v15
	global_store_dwordx4 v[10:11], v[6:9], off offset:256
	ds_read2_b32 v[10:11], v191 offset0:144 offset1:160
	s_nop 0
	v_add_u32_e32 v6, 0x90, v20
	v_mad_i64_i32 v[6:7], s[4:5], v6, s81, v[2:3]
	v_lshl_add_u64 v[12:13], v[6:7], 0, v[4:5]
	s_waitcnt lgkmcnt(0)
	v_mul_f32_e32 v6, v21, v10
	v_pk_mul_f32 v[8:9], v[88:89], v[6:7] op_sel_hi:[1,0]
	v_pk_mul_f32 v[14:15], v[86:87], v[6:7] op_sel_hi:[1,0]
	v_pk_mul_f32 v[16:17], v[84:85], v[6:7] op_sel_hi:[1,0]
	v_pk_mul_f32 v[18:19], v[82:83], v[6:7] op_sel_hi:[1,0]
	v_cvt_pk_bf16_f32 v6, v14, v15
	v_cvt_pk_bf16_f32 v7, v8, v9
	v_cvt_pk_bf16_f32 v8, v18, v19
	v_cvt_pk_bf16_f32 v9, v16, v17
	global_store_dwordx4 v[12:13], v[6:9], off
	s_nop 1
	v_mul_f32_e32 v6, v22, v10
	v_pk_mul_f32 v[8:9], v[64:65], v[6:7] op_sel_hi:[1,0]
	v_pk_mul_f32 v[14:15], v[62:63], v[6:7] op_sel_hi:[1,0]
	v_pk_mul_f32 v[16:17], v[60:61], v[6:7] op_sel_hi:[1,0]
	v_pk_mul_f32 v[18:19], v[58:59], v[6:7] op_sel_hi:[1,0]
	v_cvt_pk_bf16_f32 v6, v14, v15
	v_cvt_pk_bf16_f32 v7, v8, v9
	v_cvt_pk_bf16_f32 v8, v18, v19
	v_cvt_pk_bf16_f32 v9, v16, v17
	global_store_dwordx4 v[12:13], v[6:9], off offset:256
	s_nop 1
	v_add_u32_e32 v6, 0xa0, v20
	v_mad_i64_i32 v[6:7], s[4:5], v6, s81, v[2:3]
	v_lshl_add_u64 v[12:13], v[6:7], 0, v[4:5]
	v_mul_f32_e32 v6, v21, v11
	v_pk_mul_f32 v[8:9], v[72:73], v[6:7] op_sel_hi:[1,0]
	v_pk_mul_f32 v[14:15], v[70:71], v[6:7] op_sel_hi:[1,0]
	v_pk_mul_f32 v[16:17], v[68:69], v[6:7] op_sel_hi:[1,0]
	v_pk_mul_f32 v[18:19], v[66:67], v[6:7] op_sel_hi:[1,0]
	v_cvt_pk_bf16_f32 v6, v14, v15
	v_cvt_pk_bf16_f32 v7, v8, v9
	v_cvt_pk_bf16_f32 v8, v18, v19
	v_cvt_pk_bf16_f32 v9, v16, v17
	global_store_dwordx4 v[12:13], v[6:9], off
	s_nop 1
	v_mul_f32_e32 v6, v22, v11
	v_pk_mul_f32 v[8:9], v[48:49], v[6:7] op_sel_hi:[1,0]
	v_pk_mul_f32 v[10:11], v[46:47], v[6:7] op_sel_hi:[1,0]
	v_pk_mul_f32 v[14:15], v[44:45], v[6:7] op_sel_hi:[1,0]
	v_pk_mul_f32 v[16:17], v[42:43], v[6:7] op_sel_hi:[1,0]
	v_cvt_pk_bf16_f32 v6, v10, v11
	v_cvt_pk_bf16_f32 v7, v8, v9
	v_cvt_pk_bf16_f32 v8, v16, v17
	v_cvt_pk_bf16_f32 v9, v14, v15
	global_store_dwordx4 v[12:13], v[6:9], off offset:256
	s_nop 1
	v_add_u32_e32 v6, 0xb0, v20
	v_mad_i64_i32 v[2:3], s[4:5], v6, s81, v[2:3]
	v_lshl_add_u64 v[6:7], v[2:3], 0, v[4:5]
	v_mul_f32_e32 v2, v21, v23
	v_pk_mul_f32 v[4:5], v[56:57], v[2:3] op_sel_hi:[1,0]
	v_pk_mul_f32 v[8:9], v[54:55], v[2:3] op_sel_hi:[1,0]
	v_pk_mul_f32 v[10:11], v[52:53], v[2:3] op_sel_hi:[1,0]
	v_pk_mul_f32 v[12:13], v[50:51], v[2:3] op_sel_hi:[1,0]
	v_cvt_pk_bf16_f32 v2, v8, v9
	v_cvt_pk_bf16_f32 v3, v4, v5
	v_cvt_pk_bf16_f32 v4, v12, v13
	v_cvt_pk_bf16_f32 v5, v10, v11
	global_store_dwordx4 v[6:7], v[2:5], off
	s_nop 1
	v_mul_f32_e32 v2, v22, v23
	v_pk_mul_f32 v[4:5], v[40:41], v[2:3] op_sel_hi:[1,0]
	v_pk_mul_f32 v[8:9], v[38:39], v[2:3] op_sel_hi:[1,0]
	v_pk_mul_f32 v[10:11], v[36:37], v[2:3] op_sel_hi:[1,0]
	v_pk_mul_f32 v[12:13], v[34:35], v[2:3] op_sel_hi:[1,0]
	v_cvt_pk_bf16_f32 v2, v8, v9
	v_cvt_pk_bf16_f32 v3, v4, v5
	v_cvt_pk_bf16_f32 v4, v12, v13
	v_cvt_pk_bf16_f32 v5, v10, v11
	global_store_dwordx4 v[6:7], v[2:5], off offset:256
	s_cbranch_vccnz .LBB0_798
	s_andn2_b64 vcc, exec, s[14:15]
	s_cbranch_vccnz .LBB0_797
	s_barrier
	s_branch .LBB0_797

; __device__ __forceinline__ unsigned pk4_fp8(float a, float b, float c, float d) { int w = 0; w = __builtin_amdgcn_cvt_pk_fp8_f32(a, b, w, false); w = __builtin_amdgcn_cvt_pk_fp8_f32(c, d, w, true); return (unsigned)w; }
; #define PG8_SCHED __builtin_amdgcn_sched_barrier(0)
;     __device__ __forceinline__ void operator()(const f32x4 (&acc)[2][2][4][2], const Unit& u, int wr, int wc, int fr, int fq) const {
;         const int row0 = u.pm * BM + wr * 64 + fr, col0 = (u.pn % 28) * HALF + wc * 32 + 8 * fq;
; #pragma unroll
;         for (int ai = 0; ai < 2; ++ai)
; #pragma unroll
;             for (int m = 0; m < 4; ++m) { unsigned char* rowp = O + (size_t)(row0 + ai * HALF + m * 16) * ldc + col0;
;                 const float c1 = sc * -1.4426950408889634f, k = 1.0f / (sc * sc);
;                 const f32x4 g0 = acc[ai][0][m][0], g1 = acc[ai][0][m][1], u0 = acc[ai][1][m][0], u1 = acc[ai][1][m][1];
;                 const f32x2 o0 = silu_mul2(g0.xy, u0.xy, c1, k), o1 = silu_mul2(g0.zw, u0.zw, c1, k), o2 = silu_mul2(g1.xy, u1.xy, c1, k), o3 = silu_mul2(g1.zw, u1.zw, c1, k);
;                 u32x2 w; w.x = pk4_fp8(o0[0], o0[1], o1[0], o1[1]); w.y = pk4_fp8(o2[0], o2[1], o3[0], o3[1]);
;                 *(u32x2*)rowp = w; }
; template <class Epi, class Sched, bool ALIGN_EPI = false, bool SP2 = false, bool F8 = false>
; __device__ __forceinline__ void gemm_phase(PG8_LAS unsigned char* lds, const Gemm g, const Sched& S, const Epi& E) {
;     ...
;         if constexpr (F8) { asm volatile("s_nop 15\n\ts_nop 15" ::: "memory"); PG8_SCHED; }
.LBB0_1313:
	s_nop 7
	v_pk_mul_f32 v[2:3], v[158:159], s[18:19] op_sel_hi:[1,0]
	v_pk_mul_f32 v[12:13], v[158:159], v[154:155]
	v_exp_f32_e32 v4, v2
	v_exp_f32_e32 v5, v3
	v_pk_mul_f32 v[14:15], v[150:151], s[18:19] op_sel_hi:[1,0]
	v_pk_mul_f32 v[16:17], v[152:153], s[18:19] op_sel_hi:[1,0]
	v_exp_f32_e32 v14, v14
	v_pk_fma_f32 v[4:5], v[4:5], s[20:21], s[20:21] op_sel_hi:[1,0,0]
	v_exp_f32_e32 v15, v15
	v_rcp_f32_e32 v8, v4
	v_rcp_f32_e32 v9, v5
	v_exp_f32_e32 v16, v16
	v_pk_fma_f32 v[14:15], v[14:15], s[20:21], s[20:21] op_sel_hi:[1,0,0]
	v_exp_f32_e32 v17, v17
	v_pk_mul_f32 v[8:9], v[8:9], v[12:13]
	v_pk_mul_f32 v[12:13], v[160:161], s[18:19] op_sel_hi:[1,0]
	v_rcp_f32_e32 v14, v14
	v_exp_f32_e32 v12, v12
	v_exp_f32_e32 v13, v13
	v_rcp_f32_e32 v15, v15
	v_pk_mul_f32 v[10:11], v[160:161], v[156:157]
	s_mul_hi_i32 s0, s40, 0x92492493
	v_pk_fma_f32 v[12:13], v[12:13], s[20:21], s[20:21] op_sel_hi:[1,0,0]
	s_add_i32 s0, s0, s40
	v_rcp_f32_e32 v12, v12
	v_rcp_f32_e32 v13, v13
	s_lshr_b32 s1, s0, 31
	s_lshr_b32 s0, s0, 4
	s_add_i32 s0, s0, s1
	v_pk_mul_f32 v[10:11], v[12:13], v[10:11]
	v_pk_mul_f32 v[12:13], v[150:151], v[146:147]
	s_mul_i32 s0, s0, 28
	v_pk_mul_f32 v[12:13], v[14:15], v[12:13]
	v_pk_fma_f32 v[14:15], v[16:17], s[20:21], s[20:21] op_sel_hi:[1,0,0]
	v_mov_b32_e32 v17, 0
	v_rcp_f32_e32 v14, v14
	v_rcp_f32_e32 v15, v15
	v_cvt_pk_fp8_f32 v17, v12, v13
	v_mov_b32_e32 v16, 0
	v_cvt_pk_fp8_f32 v16, v8, v9
	v_pk_mul_f32 v[8:9], v[152:153], v[148:149]
	v_pk_mul_f32 v[12:13], v[142:143], v[138:139]
	v_pk_mul_f32 v[8:9], v[14:15], v[8:9]
	v_pk_mul_f32 v[14:15], v[134:135], s[18:19] op_sel_hi:[1,0]
	v_cvt_pk_fp8_f32 v17, v8, v9 op_sel:[0,0,1]
	v_pk_mul_f32 v[8:9], v[142:143], s[18:19] op_sel_hi:[1,0]
	s_sub_i32 s0, s40, s0
	v_exp_f32_e32 v8, v8
	v_exp_f32_e32 v9, v9
	v_cvt_pk_fp8_f32 v16, v10, v11 op_sel:[0,0,1]
	v_exp_f32_e32 v14, v14
	v_exp_f32_e32 v15, v15
	v_pk_fma_f32 v[8:9], v[8:9], s[20:21], s[20:21] op_sel_hi:[1,0,0]
	v_lshl_add_u32 v6, s38, 8, v1
	v_rcp_f32_e32 v8, v8
	v_rcp_f32_e32 v9, v9
	v_lshl_or_b32 v2, s0, 7, v185
	v_mov_b64_e32 v[4:5], s[12:13]
	v_ashrrev_i32_e32 v3, 31, v2
	v_pk_mul_f32 v[8:9], v[8:9], v[12:13]
	v_pk_mul_f32 v[12:13], v[144:145], s[18:19] op_sel_hi:[1,0]
	v_mad_i64_i32 v[10:11], s[4:5], v6, s76, v[4:5]
	v_exp_f32_e32 v12, v12
	v_exp_f32_e32 v13, v13
	v_lshl_add_u64 v[10:11], v[10:11], 0, v[2:3]
	global_store_dwordx2 v[10:11], v[16:17], off
	v_pk_fma_f32 v[14:15], v[14:15], s[20:21], s[20:21] op_sel_hi:[1,0,0]
	v_pk_fma_f32 v[12:13], v[12:13], s[20:21], s[20:21] op_sel_hi:[1,0,0]
	v_pk_mul_f32 v[16:17], v[136:137], s[18:19] op_sel_hi:[1,0]
	v_rcp_f32_e32 v12, v12
	v_rcp_f32_e32 v13, v13
	v_rcp_f32_e32 v14, v14
	v_rcp_f32_e32 v15, v15
	v_exp_f32_e32 v16, v16
	v_exp_f32_e32 v17, v17
	v_pk_mul_f32 v[10:11], v[144:145], v[140:141]
	v_or_b32_e32 v7, 16, v6
	v_pk_mul_f32 v[10:11], v[12:13], v[10:11]
	v_pk_mul_f32 v[12:13], v[134:135], v[130:131]
	s_andn2_b64 vcc, exec, s[22:23]
	v_pk_mul_f32 v[12:13], v[14:15], v[12:13]
	v_pk_fma_f32 v[14:15], v[16:17], s[20:21], s[20:21] op_sel_hi:[1,0,0]
	v_mov_b32_e32 v17, 0
	v_rcp_f32_e32 v14, v14
	v_rcp_f32_e32 v15, v15
	v_cvt_pk_fp8_f32 v17, v12, v13
	v_mov_b32_e32 v16, 0
	v_cvt_pk_fp8_f32 v16, v8, v9
	v_pk_mul_f32 v[8:9], v[136:137], v[132:133]
	v_pk_mul_f32 v[12:13], v[126:127], v[122:123]
	v_pk_mul_f32 v[8:9], v[14:15], v[8:9]
	v_pk_mul_f32 v[14:15], v[118:119], s[18:19] op_sel_hi:[1,0]
	v_cvt_pk_fp8_f32 v17, v8, v9 op_sel:[0,0,1]
	v_pk_mul_f32 v[8:9], v[126:127], s[18:19] op_sel_hi:[1,0]
	v_cvt_pk_fp8_f32 v16, v10, v11 op_sel:[0,0,1]
	v_exp_f32_e32 v8, v8
	v_exp_f32_e32 v9, v9
	v_exp_f32_e32 v14, v14
	v_exp_f32_e32 v15, v15
	v_mad_i64_i32 v[10:11], s[4:5], v7, s76, v[4:5]
	v_pk_fma_f32 v[8:9], v[8:9], s[20:21], s[20:21] op_sel_hi:[1,0,0]
	v_lshl_add_u64 v[10:11], v[10:11], 0, v[2:3]
	v_rcp_f32_e32 v8, v8
	v_rcp_f32_e32 v9, v9
	global_store_dwordx2 v[10:11], v[16:17], off
	v_pk_fma_f32 v[14:15], v[14:15], s[20:21], s[20:21] op_sel_hi:[1,0,0]
	v_pk_mul_f32 v[16:17], v[120:121], s[18:19] op_sel_hi:[1,0]
	v_pk_mul_f32 v[8:9], v[8:9], v[12:13]
	v_pk_mul_f32 v[12:13], v[128:129], s[18:19] op_sel_hi:[1,0]
	v_rcp_f32_e32 v14, v14
	v_exp_f32_e32 v12, v12
	v_exp_f32_e32 v13, v13
	v_rcp_f32_e32 v15, v15
	v_exp_f32_e32 v16, v16
	v_exp_f32_e32 v17, v17
	v_pk_fma_f32 v[12:13], v[12:13], s[20:21], s[20:21] op_sel_hi:[1,0,0]
	v_pk_mul_f32 v[10:11], v[128:129], v[124:125]
	v_rcp_f32_e32 v12, v12
	v_rcp_f32_e32 v13, v13
	v_or_b32_e32 v7, 32, v6
	s_mov_b64 s[22:23], -1
	v_pk_mul_f32 v[10:11], v[12:13], v[10:11]
	v_pk_mul_f32 v[12:13], v[118:119], v[114:115]
	s_nop 0
	v_pk_mul_f32 v[12:13], v[14:15], v[12:13]
	v_pk_fma_f32 v[14:15], v[16:17], s[20:21], s[20:21] op_sel_hi:[1,0,0]
	v_mov_b32_e32 v17, 0
	v_rcp_f32_e32 v14, v14
	v_rcp_f32_e32 v15, v15
	v_cvt_pk_fp8_f32 v17, v12, v13
	v_mov_b32_e32 v16, 0
	v_cvt_pk_fp8_f32 v16, v8, v9
	v_pk_mul_f32 v[8:9], v[120:121], v[116:117]
	v_pk_mul_f32 v[12:13], v[110:111], v[106:107]
	v_pk_mul_f32 v[8:9], v[14:15], v[8:9]
	v_pk_mul_f32 v[14:15], v[102:103], s[18:19] op_sel_hi:[1,0]
	v_cvt_pk_fp8_f32 v17, v8, v9 op_sel:[0,0,1]
	v_pk_mul_f32 v[8:9], v[110:111], s[18:19] op_sel_hi:[1,0]
	v_cvt_pk_fp8_f32 v16, v10, v11 op_sel:[0,0,1]
	v_exp_f32_e32 v8, v8
	v_exp_f32_e32 v9, v9
	v_exp_f32_e32 v14, v14
	v_exp_f32_e32 v15, v15
	v_mad_i64_i32 v[10:11], s[4:5], v7, s76, v[4:5]
	v_pk_fma_f32 v[8:9], v[8:9], s[20:21], s[20:21] op_sel_hi:[1,0,0]
	v_lshl_add_u64 v[10:11], v[10:11], 0, v[2:3]
	v_rcp_f32_e32 v8, v8
	v_rcp_f32_e32 v9, v9
	global_store_dwordx2 v[10:11], v[16:17], off
	v_pk_fma_f32 v[14:15], v[14:15], s[20:21], s[20:21] op_sel_hi:[1,0,0]
; __device__ __forceinline__ unsigned pk4_fp8(float a, float b, float c, float d) { int w = 0; w = __builtin_amdgcn_cvt_pk_fp8_f32(a, b, w, false); w = __builtin_amdgcn_cvt_pk_fp8_f32(c, d, w, true); return (unsigned)w; }
; __device__ __forceinline__ float silu_mul(float g, float u) { return g * __builtin_amdgcn_rcpf(1.0f + __builtin_amdgcn_exp2f(g * -1.4426950408889634f)) * u; }
; __device__ __forceinline__ f32x2 silu_mul2(f32x2 g, f32x2 u, float c1, float k) {
;     const f32x2 a = g * c1; f32x2 e; e[0] = __builtin_amdgcn_exp2f(a[0]); e[1] = __builtin_amdgcn_exp2f(a[1]);
;     const f32x2 kk = {k, k}; const f32x2 d = __builtin_elementwise_fma(e, kk, kk); f32x2 r; r[0] = __builtin_amdgcn_rcpf(d[0]); r[1] = __builtin_amdgcn_rcpf(d[1]);
;     return (g * u) * r;
; }
;     __device__ __forceinline__ void operator()(const f32x4 (&acc)[2][2][4][2], const Unit& u, int wr, int wc, int fr, int fq) const {
;     ...
;             for (int m = 0; m < 4; ++m) { unsigned char* rowp = O + (size_t)(row0 + ai * HALF + m * 16) * ldc + col0;
;                 const float c1 = sc * -1.4426950408889634f, k = 1.0f / (sc * sc);
;                 const f32x4 g0 = acc[ai][0][m][0], g1 = acc[ai][0][m][1], u0 = acc[ai][1][m][0], u1 = acc[ai][1][m][1];
;                 const f32x2 o0 = silu_mul2(g0.xy, u0.xy, c1, k), o1 = silu_mul2(g0.zw, u0.zw, c1, k), o2 = silu_mul2(g1.xy, u1.xy, c1, k), o3 = silu_mul2(g1.zw, u1.zw, c1, k);
;                 u32x2 w; w.x = pk4_fp8(o0[0], o0[1], o1[0], o1[1]); w.y = pk4_fp8(o2[0], o2[1], o3[0], o3[1]);
;                 *(u32x2*)rowp = w; }
	v_pk_mul_f32 v[16:17], v[104:105], s[18:19] op_sel_hi:[1,0]
	v_pk_mul_f32 v[8:9], v[8:9], v[12:13]
	v_pk_mul_f32 v[12:13], v[112:113], s[18:19] op_sel_hi:[1,0]
	v_rcp_f32_e32 v14, v14
	v_exp_f32_e32 v12, v12
	v_exp_f32_e32 v13, v13
	v_rcp_f32_e32 v15, v15
	v_exp_f32_e32 v16, v16
	v_exp_f32_e32 v17, v17
	v_pk_fma_f32 v[12:13], v[12:13], s[20:21], s[20:21] op_sel_hi:[1,0,0]
	v_pk_mul_f32 v[10:11], v[112:113], v[108:109]
	v_rcp_f32_e32 v12, v12
	v_rcp_f32_e32 v13, v13
	v_or_b32_e32 v7, 48, v6
	v_pk_mul_f32 v[10:11], v[12:13], v[10:11]
	v_pk_mul_f32 v[12:13], v[102:103], v[98:99]
	s_nop 0
	v_pk_mul_f32 v[12:13], v[14:15], v[12:13]
	v_pk_fma_f32 v[14:15], v[16:17], s[20:21], s[20:21] op_sel_hi:[1,0,0]
	v_mov_b32_e32 v17, 0
	v_rcp_f32_e32 v14, v14
	v_rcp_f32_e32 v15, v15
	v_cvt_pk_fp8_f32 v17, v12, v13
	v_mov_b32_e32 v16, 0
	v_cvt_pk_fp8_f32 v16, v8, v9
	v_pk_mul_f32 v[8:9], v[104:105], v[100:101]
	v_pk_mul_f32 v[12:13], v[94:95], v[90:91]
	v_pk_mul_f32 v[8:9], v[14:15], v[8:9]
	v_pk_mul_f32 v[14:15], v[86:87], s[18:19] op_sel_hi:[1,0]
	v_cvt_pk_fp8_f32 v17, v8, v9 op_sel:[0,0,1]
	v_pk_mul_f32 v[8:9], v[94:95], s[18:19] op_sel_hi:[1,0]
	v_cvt_pk_fp8_f32 v16, v10, v11 op_sel:[0,0,1]
	v_exp_f32_e32 v8, v8
	v_exp_f32_e32 v9, v9
	v_exp_f32_e32 v14, v14
	v_exp_f32_e32 v15, v15
	v_mad_i64_i32 v[10:11], s[4:5], v7, s76, v[4:5]
	v_pk_fma_f32 v[8:9], v[8:9], s[20:21], s[20:21] op_sel_hi:[1,0,0]
	v_lshl_add_u64 v[10:11], v[10:11], 0, v[2:3]
	v_rcp_f32_e32 v8, v8
	v_rcp_f32_e32 v9, v9
	global_store_dwordx2 v[10:11], v[16:17], off
	v_pk_fma_f32 v[14:15], v[14:15], s[20:21], s[20:21] op_sel_hi:[1,0,0]
	v_pk_mul_f32 v[16:17], v[88:89], s[18:19] op_sel_hi:[1,0]
	v_pk_mul_f32 v[8:9], v[8:9], v[12:13]
	v_pk_mul_f32 v[12:13], v[96:97], s[18:19] op_sel_hi:[1,0]
	v_rcp_f32_e32 v14, v14
	v_exp_f32_e32 v12, v12
	v_exp_f32_e32 v13, v13
	v_rcp_f32_e32 v15, v15
	v_exp_f32_e32 v16, v16
	v_exp_f32_e32 v17, v17
	v_pk_fma_f32 v[12:13], v[12:13], s[20:21], s[20:21] op_sel_hi:[1,0,0]
	v_pk_mul_f32 v[10:11], v[96:97], v[92:93]
	v_rcp_f32_e32 v12, v12
	v_rcp_f32_e32 v13, v13
	v_add_u32_e32 v7, 0x80, v6
	v_pk_mul_f32 v[10:11], v[12:13], v[10:11]
	v_pk_mul_f32 v[12:13], v[86:87], v[82:83]
	s_nop 0
	v_pk_mul_f32 v[12:13], v[14:15], v[12:13]
	v_pk_fma_f32 v[14:15], v[16:17], s[20:21], s[20:21] op_sel_hi:[1,0,0]
	v_mov_b32_e32 v17, 0
	v_rcp_f32_e32 v14, v14
	v_rcp_f32_e32 v15, v15
	v_cvt_pk_fp8_f32 v17, v12, v13
	v_mov_b32_e32 v16, 0
	v_cvt_pk_fp8_f32 v16, v8, v9
	v_pk_mul_f32 v[8:9], v[88:89], v[84:85]
	v_pk_mul_f32 v[12:13], v[78:79], v[74:75]
	v_pk_mul_f32 v[8:9], v[14:15], v[8:9]
	v_pk_mul_f32 v[14:15], v[70:71], s[18:19] op_sel_hi:[1,0]
	v_cvt_pk_fp8_f32 v17, v8, v9 op_sel:[0,0,1]
	v_pk_mul_f32 v[8:9], v[78:79], s[18:19] op_sel_hi:[1,0]
	v_cvt_pk_fp8_f32 v16, v10, v11 op_sel:[0,0,1]
	v_exp_f32_e32 v8, v8
	v_exp_f32_e32 v9, v9
	v_exp_f32_e32 v14, v14
	v_exp_f32_e32 v15, v15
	v_mad_i64_i32 v[10:11], s[4:5], v7, s76, v[4:5]
	v_pk_fma_f32 v[8:9], v[8:9], s[20:21], s[20:21] op_sel_hi:[1,0,0]
	v_lshl_add_u64 v[10:11], v[10:11], 0, v[2:3]
	v_rcp_f32_e32 v8, v8
	v_rcp_f32_e32 v9, v9
	global_store_dwordx2 v[10:11], v[16:17], off
	v_pk_fma_f32 v[14:15], v[14:15], s[20:21], s[20:21] op_sel_hi:[1,0,0]
	v_pk_mul_f32 v[16:17], v[72:73], s[18:19] op_sel_hi:[1,0]
	v_pk_mul_f32 v[8:9], v[8:9], v[12:13]
	v_pk_mul_f32 v[12:13], v[80:81], s[18:19] op_sel_hi:[1,0]
	v_rcp_f32_e32 v14, v14
	v_exp_f32_e32 v12, v12
	v_exp_f32_e32 v13, v13
	v_rcp_f32_e32 v15, v15
	v_exp_f32_e32 v16, v16
	v_exp_f32_e32 v17, v17
	v_pk_fma_f32 v[12:13], v[12:13], s[20:21], s[20:21] op_sel_hi:[1,0,0]
	v_pk_mul_f32 v[10:11], v[80:81], v[76:77]
	v_rcp_f32_e32 v12, v12
	v_rcp_f32_e32 v13, v13
	v_add_u32_e32 v7, 0x90, v6
	v_pk_mul_f32 v[10:11], v[12:13], v[10:11]
	v_pk_mul_f32 v[12:13], v[70:71], v[66:67]
	s_nop 0
	v_pk_mul_f32 v[12:13], v[14:15], v[12:13]
; __device__ __forceinline__ unsigned pk4_fp8(float a, float b, float c, float d) { int w = 0; w = __builtin_amdgcn_cvt_pk_fp8_f32(a, b, w, false); w = __builtin_amdgcn_cvt_pk_fp8_f32(c, d, w, true); return (unsigned)w; }
; #define PG8_BAR __builtin_amdgcn_s_barrier()
;     __device__ __forceinline__ void operator()(const f32x4 (&acc)[2][2][4][2], const Unit& u, int wr, int wc, int fr, int fq) const {
;     ...
;             for (int m = 0; m < 4; ++m) { unsigned char* rowp = O + (size_t)(row0 + ai * HALF + m * 16) * ldc + col0;
;                 const float c1 = sc * -1.4426950408889634f, k = 1.0f / (sc * sc);
;                 const f32x4 g0 = acc[ai][0][m][0], g1 = acc[ai][0][m][1], u0 = acc[ai][1][m][0], u1 = acc[ai][1][m][1];
;                 const f32x2 o0 = silu_mul2(g0.xy, u0.xy, c1, k), o1 = silu_mul2(g0.zw, u0.zw, c1, k), o2 = silu_mul2(g1.xy, u1.xy, c1, k), o3 = silu_mul2(g1.zw, u1.zw, c1, k);
;                 u32x2 w; w.x = pk4_fp8(o0[0], o0[1], o1[0], o1[1]); w.y = pk4_fp8(o2[0], o2[1], o3[0], o3[1]);
;                 *(u32x2*)rowp = w; }
; template <class Epi, class Sched, bool ALIGN_EPI = false, bool SP2 = false, bool F8 = false>
; __device__ __forceinline__ void gemm_phase(PG8_LAS unsigned char* lds, const Gemm g, const Sched& S, const Epi& E) {
;     ...
;         if (!has_next) break;
; #pragma unroll
;         for (int a = 0; a < 2; ++a)
; #pragma unroll
;             for (int b = 0; b < 2; ++b)
; #pragma unroll
;                 for (int m = 0; m < 4; ++m)
; #pragma unroll
;                     for (int n = 0; n < 2; ++n) acc[a][b][m][n] = (f32x4){0.f, 0.f, 0.f, 0.f};
;         cur = nxt; cA = nA; cB = nB; ++ui;
;         if constexpr (ALIGN_EPI) { if (wr == 1) PG8_BAR; }
	v_pk_fma_f32 v[14:15], v[16:17], s[20:21], s[20:21] op_sel_hi:[1,0,0]
	v_mov_b32_e32 v17, 0
	v_rcp_f32_e32 v14, v14
	v_rcp_f32_e32 v15, v15
	v_cvt_pk_fp8_f32 v17, v12, v13
	v_mov_b32_e32 v16, 0
	v_cvt_pk_fp8_f32 v16, v8, v9
	v_pk_mul_f32 v[8:9], v[72:73], v[68:69]
	v_pk_mul_f32 v[12:13], v[62:63], v[58:59]
	v_pk_mul_f32 v[8:9], v[14:15], v[8:9]
	v_pk_mul_f32 v[14:15], v[54:55], s[18:19] op_sel_hi:[1,0]
	v_cvt_pk_fp8_f32 v17, v8, v9 op_sel:[0,0,1]
	v_pk_mul_f32 v[8:9], v[62:63], s[18:19] op_sel_hi:[1,0]
	v_cvt_pk_fp8_f32 v16, v10, v11 op_sel:[0,0,1]
	v_exp_f32_e32 v8, v8
	v_exp_f32_e32 v9, v9
	v_exp_f32_e32 v14, v14
	v_exp_f32_e32 v15, v15
	v_mad_i64_i32 v[10:11], s[4:5], v7, s76, v[4:5]
	v_pk_fma_f32 v[8:9], v[8:9], s[20:21], s[20:21] op_sel_hi:[1,0,0]
	v_lshl_add_u64 v[10:11], v[10:11], 0, v[2:3]
	v_rcp_f32_e32 v8, v8
	v_rcp_f32_e32 v9, v9
	global_store_dwordx2 v[10:11], v[16:17], off
	v_pk_fma_f32 v[14:15], v[14:15], s[20:21], s[20:21] op_sel_hi:[1,0,0]
	v_pk_mul_f32 v[16:17], v[56:57], s[18:19] op_sel_hi:[1,0]
	v_pk_mul_f32 v[8:9], v[8:9], v[12:13]
	v_pk_mul_f32 v[12:13], v[64:65], s[18:19] op_sel_hi:[1,0]
	v_rcp_f32_e32 v14, v14
	v_exp_f32_e32 v12, v12
	v_exp_f32_e32 v13, v13
	v_rcp_f32_e32 v15, v15
	v_exp_f32_e32 v16, v16
	v_exp_f32_e32 v17, v17
	v_pk_fma_f32 v[12:13], v[12:13], s[20:21], s[20:21] op_sel_hi:[1,0,0]
	v_pk_mul_f32 v[10:11], v[64:65], v[60:61]
	v_rcp_f32_e32 v12, v12
	v_rcp_f32_e32 v13, v13
	v_add_u32_e32 v7, 0xa0, v6
	v_pk_mul_f32 v[10:11], v[12:13], v[10:11]
	v_pk_mul_f32 v[12:13], v[54:55], v[50:51]
	s_nop 0
	v_pk_mul_f32 v[12:13], v[14:15], v[12:13]
	v_pk_fma_f32 v[14:15], v[16:17], s[20:21], s[20:21] op_sel_hi:[1,0,0]
	v_mov_b32_e32 v17, 0
	v_rcp_f32_e32 v14, v14
	v_rcp_f32_e32 v15, v15
	v_cvt_pk_fp8_f32 v17, v12, v13
	v_mov_b32_e32 v16, 0
	v_cvt_pk_fp8_f32 v16, v8, v9
	v_pk_mul_f32 v[8:9], v[56:57], v[52:53]
	v_pk_mul_f32 v[12:13], v[38:39], s[18:19] op_sel_hi:[1,0]
	v_pk_mul_f32 v[8:9], v[14:15], v[8:9]
	v_cvt_pk_fp8_f32 v16, v10, v11 op_sel:[0,0,1]
	v_cvt_pk_fp8_f32 v17, v8, v9 op_sel:[0,0,1]
	v_pk_mul_f32 v[8:9], v[46:47], s[18:19] op_sel_hi:[1,0]
	v_mad_i64_i32 v[10:11], s[4:5], v7, s76, v[4:5]
	v_exp_f32_e32 v8, v8
	v_exp_f32_e32 v9, v9
	v_lshl_add_u64 v[10:11], v[10:11], 0, v[2:3]
	global_store_dwordx2 v[10:11], v[16:17], off
	v_pk_mul_f32 v[10:11], v[46:47], v[42:43]
	v_pk_fma_f32 v[8:9], v[8:9], s[20:21], s[20:21] op_sel_hi:[1,0,0]
	v_exp_f32_e32 v12, v12
	v_rcp_f32_e32 v8, v8
	v_rcp_f32_e32 v9, v9
	v_exp_f32_e32 v13, v13
	v_pk_mul_f32 v[14:15], v[40:41], s[18:19] op_sel_hi:[1,0]
	v_add_u32_e32 v16, 0xb0, v6
	v_pk_mul_f32 v[8:9], v[8:9], v[10:11]
	v_pk_mul_f32 v[10:11], v[48:49], s[18:19] op_sel_hi:[1,0]
	v_pk_fma_f32 v[12:13], v[12:13], s[20:21], s[20:21] op_sel_hi:[1,0,0]
	v_exp_f32_e32 v10, v10
	v_exp_f32_e32 v11, v11
	v_rcp_f32_e32 v12, v12
	v_rcp_f32_e32 v13, v13
	v_exp_f32_e32 v14, v14
	v_pk_fma_f32 v[10:11], v[10:11], s[20:21], s[20:21] op_sel_hi:[1,0,0]
	v_exp_f32_e32 v15, v15
	v_rcp_f32_e32 v10, v10
	v_rcp_f32_e32 v11, v11
	v_pk_mul_f32 v[6:7], v[48:49], v[44:45]
	v_mad_i64_i32 v[4:5], s[4:5], v16, s76, v[4:5]
	v_pk_mul_f32 v[6:7], v[10:11], v[6:7]
	v_pk_mul_f32 v[10:11], v[38:39], v[34:35]
	v_lshl_add_u64 v[2:3], v[4:5], 0, v[2:3]
	v_pk_mul_f32 v[10:11], v[12:13], v[10:11]
	v_pk_fma_f32 v[12:13], v[14:15], s[20:21], s[20:21] op_sel_hi:[1,0,0]
	v_mov_b32_e32 v14, 0
	v_rcp_f32_e32 v12, v12
	v_rcp_f32_e32 v13, v13
	v_mov_b32_e32 v15, 0
	v_cvt_pk_fp8_f32 v14, v8, v9
	v_cvt_pk_fp8_f32 v15, v10, v11
	v_pk_mul_f32 v[8:9], v[40:41], v[36:37]
	v_cvt_pk_fp8_f32 v14, v6, v7 op_sel:[0,0,1]
	v_pk_mul_f32 v[8:9], v[12:13], v[8:9]
	s_nop 0
	v_cvt_pk_fp8_f32 v15, v8, v9 op_sel:[0,0,1]
	global_store_dwordx2 v[2:3], v[14:15], off
	s_cbranch_vccnz .LBB0_1306
	s_andn2_b64 vcc, exec, s[10:11]
	s_cbranch_vccnz .LBB0_1305
	s_barrier
	s_branch .LBB0_1305

; __device__ __forceinline__ unsigned pk4_fp8(float a, float b, float c, float d) { int w = 0; w = __builtin_amdgcn_cvt_pk_fp8_f32(a, b, w, false); w = __builtin_amdgcn_cvt_pk_fp8_f32(c, d, w, true); return (unsigned)w; }
; #define PG8_SCHED __builtin_amdgcn_sched_barrier(0)
;     __device__ __forceinline__ void operator()(const f32x4 (&acc)[2][2][4][2], const Unit& u, int wr, int wc, int fr, int fq) const {
;         const int rl0 = ui * BM + wr * 64 + fr, col0 = (u.pn & 3) * BM + wc * 32 + 8 * fq;
; #pragma unroll
;         for (int ai = 0; ai < 2; ++ai)
; #pragma unroll
;             for (int m = 0; m < 4; ++m) { const int rl = rl0 + ai * HALF + m * 16; const int d = dtab[rl];
;                 if (d >= 0) { const float gt = gtab[rl]; unsigned char* rowp = O + (size_t)d * 1024 + col0;
; #pragma unroll
;                     for (int bj = 0; bj < 2; ++bj) { const f32x4 v0 = acc[ai][bj][m][0] * gt, v1 = acc[ai][bj][m][1] * gt;
;                         u32x2 w; w.x = pk4_fp8(v0[0], v0[1], v0[2], v0[3]); w.y = pk4_fp8(v1[0], v1[1], v1[2], v1[3]);
;                         *(u32x2*)(rowp + bj * HALF) = w; } } }
; template <class Epi, class Sched, bool ALIGN_EPI = false, bool SP2 = false, bool F8 = false>
; __device__ __forceinline__ void gemm_phase(PG8_LAS unsigned char* lds, const Gemm g, const Sched& S, const Epi& E) {
;     ...
;         if constexpr (F8) { asm volatile("s_nop 15\n\ts_nop 15" ::: "memory"); PG8_SCHED; }
.LBB0_1395:
	s_nop 7
	v_lshl_add_u32 v6, s75, 8, v1
	v_lshl_add_u32 v4, v6, 2, 0
	v_add_u32_e32 v5, 0x21540, v4
	ds_read_b32 v2, v5
	v_lshlrev_b32_e32 v3, 8, v199
	v_and_b32_e32 v3, 0x300, v3
	v_or_b32_e32 v172, v3, v163
	s_waitcnt lgkmcnt(0)
	v_cmp_lt_i32_e32 vcc, -1, v2
	s_and_saveexec_b64 s[30:31], vcc
	s_cbranch_execz .LBB0_1397
	v_add_u32_e32 v3, 0x21d40, v4
	ds_read_b32 v8, v3
	v_mov_b32_e32 v10, v173
	v_mov_b32_e32 v11, v173
	v_mov_b32_e32 v16, v173
	v_mov_b32_e32 v17, v173
	s_waitcnt lgkmcnt(0)
	v_pk_mul_f32 v[12:13], v[158:159], v[8:9] op_sel_hi:[1,0]
	v_pk_mul_f32 v[14:15], v[154:155], v[8:9] op_sel_hi:[1,0]
	v_cvt_pk_fp8_f32 v10, v12, v13
	v_cvt_pk_fp8_f32 v11, v14, v15
	v_pk_mul_f32 v[12:13], v[160:161], v[8:9] op_sel_hi:[1,0]
	v_pk_mul_f32 v[14:15], v[156:157], v[8:9] op_sel_hi:[1,0]
	v_cvt_pk_fp8_f32 v10, v12, v13 op_sel:[0,0,1]
	v_cvt_pk_fp8_f32 v11, v14, v15 op_sel:[0,0,1]
	v_pk_mul_f32 v[12:13], v[150:151], v[8:9] op_sel_hi:[1,0]
	v_pk_mul_f32 v[14:15], v[146:147], v[8:9] op_sel_hi:[1,0]
	v_cvt_pk_fp8_f32 v16, v12, v13
	v_cvt_pk_fp8_f32 v17, v14, v15
	v_mov_b32_e32 v3, v173
	v_pk_mul_f32 v[12:13], v[152:153], v[8:9] op_sel_hi:[1,0]
	v_pk_mul_f32 v[8:9], v[148:149], v[8:9] op_sel_hi:[1,0]
	v_lshlrev_b64 v[2:3], 10, v[2:3]
	v_cvt_pk_fp8_f32 v16, v12, v13 op_sel:[0,0,1]
	v_cvt_pk_fp8_f32 v17, v8, v9 op_sel:[0,0,1]
	v_lshl_add_u64 v[2:3], s[16:17], 0, v[2:3]
	v_lshl_add_u64 v[2:3], v[2:3], 0, v[172:173]
	global_store_dwordx2 v[2:3], v[10:11], off
	global_store_dwordx2 v[2:3], v[16:17], off offset:128

; #define PG8_WAIT_V(n) asm volatile("s_waitcnt vmcnt(" #n ")" ::: "memory")
; #define PG8_BAR __builtin_amdgcn_s_barrier()
; #define PG8_SCHED __builtin_amdgcn_sched_barrier(0)
;     __device__ __forceinline__ void operator()(const f32x4 (&acc)[2][2][4][2], const Unit& u, int wr, int wc, int fr, int fq) const {
;         float* tile = part + (size_t)(((u.pm - 128) * 4 + (u.pn & 3)) * 7 + u.ko / 512) * 65536 + wc * 32 + 4 * fq;
; #pragma unroll
;         for (int ai = 0; ai < 2; ++ai)
; #pragma unroll
;             for (int m = 0; m < 4; ++m) { float* rowp = tile + (ai * HALF + wr * 64 + m * 16 + fr) * 256;
; #pragma unroll
;                 for (int bj = 0; bj < 2; ++bj)
; #pragma unroll
;                     for (int n = 0; n < 2; ++n) *(f32x4*)(rowp + bj * HALF + n * 16) = acc[ai][bj][m][n]; }
; template <class Epi, class Sched, bool ALIGN_EPI = false, bool SP2 = false, bool F8 = false>
; __device__ __forceinline__ void gemm_phase(PG8_LAS unsigned char* lds, const Gemm g, const Sched& S, const Epi& E) {
;     ...
;         if constexpr (F8) { asm volatile("s_nop 15\n\ts_nop 15" ::: "memory"); PG8_SCHED; }
;     ...
;     PG8_WAIT_V(0);
;     if constexpr (!ALIGN_EPI) { if (wr == 0) PG8_BAR; }
;     PG8_BAR;
.LBB0_1420:
	s_lshl_b32 s0, s27, 2
	v_lshlrev_b32_e32 v130, 8, v160
	s_nop 7
	s_add_u32 s4, s34, s0
	v_lshl_or_b32 v130, s22, 14, v130
	s_addc_u32 s5, s35, 0
	v_lshlrev_b32_e32 v128, 4, v161
	v_mov_b32_e32 v129, 0
	v_add_u32_e32 v132, 0x8000, v130
	v_add_u32_e32 v134, 0x9000, v130
	v_add_u32_e32 v136, 0xa000, v130
	v_add_u32_e32 v138, 0xb000, v130
	v_lshl_add_u64 v[128:129], s[4:5], 0, v[128:129]
	v_ashrrev_i32_e32 v131, 31, v130
	v_ashrrev_i32_e32 v133, 31, v132
	v_ashrrev_i32_e32 v135, 31, v134
	v_ashrrev_i32_e32 v137, 31, v136
	v_ashrrev_i32_e32 v139, 31, v138
	s_lshl_b32 s0, s24, 2
	s_and_b32 s1, s23, 3
	s_or_b32 s0, s0, s1
	s_mul_i32 s0, s0, 7
	s_add_i32 s0, s0, s25
	s_add_i32 s4, s0, 0xfffff200
	s_ashr_i32 s5, s4, 31
	s_lshl_b64 s[4:5], s[4:5], 18
	v_lshl_add_u64 v[128:129], v[128:129], 0, s[4:5]
	s_mov_b64 s[4:5], 0x18400000
	v_lshl_add_u64 v[128:129], v[128:129], 0, s[4:5]
	v_lshl_add_u64 v[130:131], v[130:131], 2, v[128:129]
	s_movk_i32 s0, 0x4000
	global_store_dwordx4 v[130:131], v[28:31], off
	global_store_dwordx4 v[130:131], v[32:35], off offset:64
	global_store_dwordx4 v[130:131], v[60:63], off offset:512
	global_store_dwordx4 v[130:131], v[64:67], off offset:576
	v_add_co_u32_e32 v28, vcc, s0, v130
	s_nop 1
	v_addc_co_u32_e32 v29, vcc, 0, v131, vcc
	global_store_dwordx4 v[28:29], v[20:23], off
	global_store_dwordx4 v[28:29], v[24:27], off offset:64
	global_store_dwordx4 v[28:29], v[52:55], off offset:512
	global_store_dwordx4 v[28:29], v[56:59], off offset:576
	v_add_co_u32_e32 v20, vcc, s3, v130
	s_nop 1
	v_addc_co_u32_e32 v21, vcc, 0, v131, vcc
	global_store_dwordx4 v[20:21], v[12:15], off
	global_store_dwordx4 v[20:21], v[16:19], off offset:64
	global_store_dwordx4 v[20:21], v[44:47], off offset:512
	global_store_dwordx4 v[20:21], v[48:51], off offset:576
	v_add_co_u32_e32 v12, vcc, s26, v130
	s_nop 1
	v_addc_co_u32_e32 v13, vcc, 0, v131, vcc
	global_store_dwordx4 v[12:13], v[4:7], off
	global_store_dwordx4 v[12:13], v[8:11], off offset:64
	global_store_dwordx4 v[12:13], v[36:39], off offset:512
	global_store_dwordx4 v[12:13], v[40:43], off offset:576
	v_lshl_add_u64 v[4:5], v[132:133], 2, v[128:129]
	global_store_dwordx4 v[4:5], v[68:71], off
	global_store_dwordx4 v[4:5], v[84:87], off offset:64
	global_store_dwordx4 v[4:5], v[116:119], off offset:512
	global_store_dwordx4 v[4:5], v[124:127], off offset:576
	v_lshl_add_u64 v[4:5], v[134:135], 2, v[128:129]
	global_store_dwordx4 v[4:5], v[72:75], off
	global_store_dwordx4 v[4:5], v[88:91], off offset:64
	global_store_dwordx4 v[4:5], v[108:111], off offset:512
	global_store_dwordx4 v[4:5], v[120:123], off offset:576
	v_lshl_add_u64 v[4:5], v[136:137], 2, v[128:129]
	global_store_dwordx4 v[4:5], v[76:79], off
	global_store_dwordx4 v[4:5], v[92:95], off offset:64
	global_store_dwordx4 v[4:5], v[104:107], off offset:512
	global_store_dwordx4 v[4:5], v[112:115], off offset:576
	v_lshl_add_u64 v[4:5], v[138:139], 2, v[128:129]
	global_store_dwordx4 v[4:5], v[80:83], off
	global_store_dwordx4 v[4:5], v[96:99], off offset:64
	global_store_dwordx4 v[4:5], v[100:103], off offset:512
	global_store_dwordx4 v[4:5], v[0:3], off offset:576
	s_waitcnt vmcnt(0)
	s_barrier
